# MoE P5/P6: skip MFMAs of all-padding row blocks per expert tile + XCD unit order with smallest tiles last
# speedup vs baseline: 1.0046x; 1.0046x over previous
; #define PG8_STAGE(bufoff, gbase, voff) do { const char* _gb = (const char*)(gbase); asm volatile("" : "+s"(_gb)); _Pragma("unroll") for (int _i = 0; _i < 2; ++_i) { unsigned _vo = (voff)[_i]; asm volatile("" : "+v"(_vo)); \
;         __builtin_amdgcn_global_load_lds((const unsigned*)(_gb + _vo), (LAS unsigned*)(lds + (bufoff) + ldsw + _i * 8192), 16, 0, 0); } } while (0)
; #define PG8_WAIT_V(n) asm volatile("s_waitcnt vmcnt(" #n ")" ::: "memory")
; #define PG8_WAIT_L(n) asm volatile("s_waitcnt lgkmcnt(" #n ")" ::: "memory")
; template <class Epi, class Sched, bool ALIGN_EPI, bool GATHER, bool F8 = false>
; __device__ __forceinline__ void gemm_phase(LAS unsigned char* lds, const Gemm g, const Sched& S, const Epi& E, const LAS int* gtok, const int tid) {
;     ...
;     for (;;) {
;         const bool has_next = S.next(ui + 1, nxt);
;         const char* nA = GATHER ? cA : (has_next ? (const char*)g.A + (size_t)nxt.pm * tstep : cA); const char* nB = has_next ? (const char*)g.Bt + (size_t)nxt.pn * tstep : cB;
; #pragma unroll 1
;         for (int t = 0; t < nt; t += 2) {
;             const bool last = (t == nt - 2);
;             const char* a1 = cA + (size_t)(t + 1) * kstep;
;             const char* a2 = last ? nA : cA + (size_t)(t + 2) * kstep; const char* b2 = last ? nB : cB + (size_t)(t + 2) * kstep;
;             const char* a3 = a2 + kstep; const char* b3 = b2 + kstep;
;             unsigned vS[2][2];
; #pragma unroll
;             for (int h = 0; h < 2; ++h)
; #pragma unroll
;                 for (int i = 0; i < 2; ++i) vS[h][i] = vA[h][i];
;             if constexpr (GATHER) { if (last && has_next) { PG8_GLOAD(vS, nxt.slot); } }
;             PG8_LDB(B0, 0, 0); PG8_LDB(B1, 0, 1); PG8_SCHED; PG8_LDA(At, 0, 0); PG8_STAGE(PG8_SA(1, 1), a1, vA[1]);
;             PG8_WAIT_V(8); PG8_WAIT_L(0); PG8_BAR; PG8_MMA(0, 0, At, B0); PG8_MMA(0, 1, At, B1); PG8_BAR; PG8_SCHED;
;     __device__ __forceinline__ void operator()(AccRef acc, const Unit& u, int wr, int wc, int fr, int fq) const {
;     ...
;             for (int m = 0; m < 4; ++m) { const size_t ro = (size_t)(row0 + ai * HALF + m * 16) * DM + col0;
;                 f32x4 xv[2][2];
; #pragma unroll
;                 for (int bj = 0; bj < 2; ++bj)
; #pragma unroll
;                     for (int n = 0; n < 2; ++n) xv[bj][n] = __builtin_nontemporal_load((const f32x4*)(X + ro + bj * HALF + 4 * n));
.LBB0_485:
	s_ashr_i32 s43, s42, 31
	s_lshl_b64 s[44:45], s[42:43], 20
	s_add_u32 s44, s8, s44
	s_addc_u32 s45, s9, s45
	s_and_b64 s[46:47], s[0:1], exec
	s_cselect_b32 s43, s45, s51
	s_cselect_b32 s85, s44, s50
	s_ashr_i32 s41, s40, 31
	s_lshl_b64 s[46:47], s[40:41], 20
	s_add_u32 s46, s57, s46
	s_addc_u32 s47, s72, s47
	s_and_b64 s[64:65], s[0:1], exec
	s_cselect_b32 s41, s47, s63
	s_cselect_b32 s86, s46, s62
	s_add_u32 s87, s62, 0x100
	v_mov_b32_e32 v32, 0
	s_addc_u32 s33, s63, 0
	s_mov_b32 s88, -2
	v_mov_b32_e32 v33, v32
	v_mov_b32_e32 v34, v32
	v_mov_b32_e32 v35, v32
	v_mov_b32_e32 v36, v32
	v_mov_b32_e32 v37, v32
	v_mov_b32_e32 v38, v32
	v_mov_b32_e32 v39, v32
	v_mov_b32_e32 v48, v32
	v_mov_b32_e32 v49, v32
	v_mov_b32_e32 v50, v32
	v_mov_b32_e32 v51, v32
	v_mov_b32_e32 v52, v32
	v_mov_b32_e32 v53, v32
	v_mov_b32_e32 v54, v32
	v_mov_b32_e32 v55, v32
	v_mov_b32_e32 v0, v32
	v_mov_b32_e32 v1, v32
	v_mov_b32_e32 v2, v32
	v_mov_b32_e32 v3, v32
	v_mov_b32_e32 v4, v32
	v_mov_b32_e32 v5, v32
	v_mov_b32_e32 v6, v32
	v_mov_b32_e32 v7, v32
	v_mov_b32_e32 v16, v32
	v_mov_b32_e32 v17, v32
	v_mov_b32_e32 v18, v32
	v_mov_b32_e32 v19, v32
	v_mov_b32_e32 v20, v32
	v_mov_b32_e32 v21, v32
	v_mov_b32_e32 v22, v32
	v_mov_b32_e32 v23, v32
	v_mov_b32_e32 v40, v32
	v_mov_b32_e32 v41, v32
	v_mov_b32_e32 v42, v32
	v_mov_b32_e32 v43, v32
	v_mov_b32_e32 v44, v32
	v_mov_b32_e32 v45, v32
	v_mov_b32_e32 v46, v32
	v_mov_b32_e32 v47, v32
	v_mov_b32_e32 v56, v32
	v_mov_b32_e32 v57, v32
	v_mov_b32_e32 v58, v32
	v_mov_b32_e32 v59, v32
	v_mov_b32_e32 v60, v32
	v_mov_b32_e32 v61, v32
	v_mov_b32_e32 v62, v32
	v_mov_b32_e32 v63, v32
	v_mov_b32_e32 v64, v32
	v_mov_b32_e32 v65, v32
	v_mov_b32_e32 v66, v32
	v_mov_b32_e32 v67, v32
	v_mov_b32_e32 v68, v32
	v_mov_b32_e32 v69, v32
	v_mov_b32_e32 v70, v32
	v_mov_b32_e32 v71, v32
	v_mov_b32_e32 v80, v32
	v_mov_b32_e32 v81, v32
	v_mov_b32_e32 v82, v32
	v_mov_b32_e32 v83, v32
	v_mov_b32_e32 v84, v32
	v_mov_b32_e32 v85, v32
	v_mov_b32_e32 v86, v32
	v_mov_b32_e32 v87, v32
	v_mov_b32_e32 v112, v32
	v_mov_b32_e32 v113, v32
	v_mov_b32_e32 v114, v32
	v_mov_b32_e32 v115, v32
	v_mov_b32_e32 v116, v32
	v_mov_b32_e32 v117, v32
	v_mov_b32_e32 v118, v32
	v_mov_b32_e32 v119, v32
	v_mov_b32_e32 v128, v32
	v_mov_b32_e32 v129, v32
	v_mov_b32_e32 v130, v32
	v_mov_b32_e32 v131, v32
	v_mov_b32_e32 v132, v32
	v_mov_b32_e32 v133, v32
	v_mov_b32_e32 v134, v32
	v_mov_b32_e32 v135, v32
	v_mov_b32_e32 v72, v32
	v_mov_b32_e32 v73, v32
	v_mov_b32_e32 v74, v32
	v_mov_b32_e32 v75, v32
	v_mov_b32_e32 v76, v32
	v_mov_b32_e32 v77, v32
	v_mov_b32_e32 v78, v32
	v_mov_b32_e32 v79, v32
	v_mov_b32_e32 v88, v32
	v_mov_b32_e32 v89, v32
	v_mov_b32_e32 v90, v32
	v_mov_b32_e32 v91, v32
	v_mov_b32_e32 v92, v32
	v_mov_b32_e32 v93, v32
	v_mov_b32_e32 v94, v32
	v_mov_b32_e32 v95, v32
	v_mov_b32_e32 v120, v32
	v_mov_b32_e32 v121, v32
	v_mov_b32_e32 v122, v32
	v_mov_b32_e32 v123, v32
	v_mov_b32_e32 v124, v32
	v_mov_b32_e32 v125, v32
	v_mov_b32_e32 v126, v32
	v_mov_b32_e32 v127, v32
	v_mov_b32_e32 v136, v32
	v_mov_b32_e32 v137, v32
	v_mov_b32_e32 v138, v32
	v_mov_b32_e32 v139, v32
	v_mov_b32_e32 v140, v32
	v_mov_b32_e32 v141, v32
	v_mov_b32_e32 v142, v32
	v_mov_b32_e32 v143, v32
	v_mov_b32_e32 v24, v32
	v_mov_b32_e32 v25, v32
	v_mov_b32_e32 v26, v32
	v_mov_b32_e32 v27, v32
	v_mov_b32_e32 v28, v32
	v_mov_b32_e32 v29, v32
	v_mov_b32_e32 v30, v32
	v_mov_b32_e32 v31, v32
	v_mov_b32_e32 v8, v32
	v_mov_b32_e32 v9, v32
	v_mov_b32_e32 v10, v32
	v_mov_b32_e32 v11, v32
	v_mov_b32_e32 v12, v32
	v_mov_b32_e32 v13, v32
	v_mov_b32_e32 v14, v32
	v_mov_b32_e32 v15, v32
.LBB0_486:
	ds_read_b128 v[96:99], v161
	ds_read_b128 v[100:103], v161 offset:1024
	ds_read_b128 v[104:107], v161 offset:2048
	ds_read_b128 v[108:111], v161 offset:3072
	ds_read_b128 v[148:151], v162
	ds_read_b128 v[164:167], v162 offset:1024
	ds_read_b128 v[168:171], v162 offset:2048
	ds_read_b128 v[172:175], v162 offset:3072
	s_add_u32 s62, s50, 0x100
	s_addc_u32 s63, s51, 0
	s_cmp_eq_u32 s88, 28
	s_cselect_b32 s68, s85, s62
	s_cselect_b32 s69, s43, s63
	s_cselect_b32 s66, s86, s87
	s_cselect_b32 s67, s41, s33
	s_add_u32 s64, s68, 0x80
	s_addc_u32 s65, s69, 0
	s_add_u32 s50, s50, 0x80
	s_addc_u32 s51, s51, 0
	v_mov_b32_e32 v152, v156
	ds_read_b128 v[176:179], v163
	ds_read_b128 v[180:183], v163 offset:1024
	ds_read_b128 v[184:187], v163 offset:2048
	ds_read_b128 v[188:191], v163 offset:3072
	ds_read_b128 v[192:195], v163 offset:4096
	ds_read_b128 v[196:199], v163 offset:5120
	ds_read_b128 v[200:203], v163 offset:6144
	ds_read_b128 v[204:207], v163 offset:7168
	s_add_i32 m0, s49, 0xc000
	s_nop 0
	global_load_lds_dwordx4 v152, s[50:51]
	v_mov_b32_e32 v152, v159
	s_add_i32 m0, s49, 0xe000
	s_nop 0
	global_load_lds_dwordx4 v152, s[50:51]
	s_waitcnt vmcnt(8)
	s_waitcnt lgkmcnt(0)
	s_barrier
; #define PG8_STAGE(bufoff, gbase, voff) do { const char* _gb = (const char*)(gbase); asm volatile("" : "+s"(_gb)); _Pragma("unroll") for (int _i = 0; _i < 2; ++_i) { unsigned _vo = (voff)[_i]; asm volatile("" : "+v"(_vo)); \
;         __builtin_amdgcn_global_load_lds((const unsigned*)(_gb + _vo), (LAS unsigned*)(lds + (bufoff) + ldsw + _i * 8192), 16, 0, 0); } } while (0)
; #define PG8_WAIT_V(n) asm volatile("s_waitcnt vmcnt(" #n ")" ::: "memory")
; #define PG8_WAIT_L(n) asm volatile("s_waitcnt lgkmcnt(" #n ")" ::: "memory")
; #define PG8_BAR __builtin_amdgcn_s_barrier()
; #define PG8_SCHED __builtin_amdgcn_sched_barrier(0)
; template <class Epi, class Sched, bool ALIGN_EPI, bool GATHER, bool F8 = false>
; __device__ __forceinline__ void gemm_phase(LAS unsigned char* lds, const Gemm g, const Sched& S, const Epi& E, const LAS int* gtok, const int tid) {
;     ...
;             PG8_WAIT_V(8); PG8_WAIT_L(0); PG8_BAR; PG8_MMA(0, 0, At, B0); PG8_MMA(0, 1, At, B1); PG8_BAR; PG8_SCHED;
;             PG8_LDA(At, 0, 1); PG8_STAGE(PG8_SB(0, 0), b2, voffB); PG8_STAGE(PG8_SB(0, 1), b2 + hstep, voffB); PG8_STAGE(PG8_SA(0, 0), a2, vS[0]);
;             PG8_WAIT_V(8); PG8_WAIT_L(0); PG8_BAR; PG8_MMA(1, 0, At, B0); PG8_MMA(1, 1, At, B1); PG8_BAR; PG8_SCHED;
	s_setprio 1
	s_waitcnt lgkmcnt(0)
	v_mfma_f32_16x16x32_bf16 v[140:143], v[96:99], v[176:179], v[140:143]
	v_mfma_f32_16x16x32_bf16 v[136:139], v[104:107], v[176:179], v[136:139]
	v_mfma_f32_16x16x32_bf16 v[124:127], v[96:99], v[184:187], v[124:127]
	v_mfma_f32_16x16x32_bf16 v[120:123], v[104:107], v[184:187], v[120:123]
	v_mfma_f32_16x16x32_bf16 v[92:95], v[96:99], v[192:195], v[92:95]
	v_mfma_f32_16x16x32_bf16 v[88:91], v[104:107], v[192:195], v[88:91]
	v_mfma_f32_16x16x32_bf16 v[76:79], v[96:99], v[200:203], v[76:79]
	v_mfma_f32_16x16x32_bf16 v[72:75], v[104:107], v[200:203], v[72:75]
	v_mfma_f32_16x16x32_bf16 v[140:143], v[100:103], v[180:183], v[140:143]
	v_mfma_f32_16x16x32_bf16 v[136:139], v[108:111], v[180:183], v[136:139]
	v_mfma_f32_16x16x32_bf16 v[124:127], v[100:103], v[188:191], v[124:127]
	v_mfma_f32_16x16x32_bf16 v[120:123], v[108:111], v[188:191], v[120:123]
	v_mfma_f32_16x16x32_bf16 v[92:95], v[100:103], v[196:199], v[92:95]
	v_mfma_f32_16x16x32_bf16 v[88:91], v[108:111], v[196:199], v[88:91]
	v_mfma_f32_16x16x32_bf16 v[76:79], v[100:103], v[204:207], v[76:79]
	v_mfma_f32_16x16x32_bf16 v[72:75], v[108:111], v[204:207], v[72:75]
	s_setprio 0
	s_setprio 1
	v_mfma_f32_16x16x32_bf16 v[132:135], v[148:151], v[176:179], v[132:135]
	v_mfma_f32_16x16x32_bf16 v[128:131], v[168:171], v[176:179], v[128:131]
	v_mfma_f32_16x16x32_bf16 v[116:119], v[148:151], v[184:187], v[116:119]
	v_mfma_f32_16x16x32_bf16 v[112:115], v[168:171], v[184:187], v[112:115]
	v_mfma_f32_16x16x32_bf16 v[84:87], v[148:151], v[192:195], v[84:87]
	v_mfma_f32_16x16x32_bf16 v[80:83], v[168:171], v[192:195], v[80:83]
	v_mfma_f32_16x16x32_bf16 v[68:71], v[148:151], v[200:203], v[68:71]
	v_mfma_f32_16x16x32_bf16 v[64:67], v[168:171], v[200:203], v[64:67]
	v_mfma_f32_16x16x32_bf16 v[132:135], v[164:167], v[180:183], v[132:135]
	v_mfma_f32_16x16x32_bf16 v[128:131], v[172:175], v[180:183], v[128:131]
	v_mfma_f32_16x16x32_bf16 v[116:119], v[164:167], v[188:191], v[116:119]
	v_mfma_f32_16x16x32_bf16 v[112:115], v[172:175], v[188:191], v[112:115]
	v_mfma_f32_16x16x32_bf16 v[84:87], v[164:167], v[196:199], v[84:87]
	v_mfma_f32_16x16x32_bf16 v[80:83], v[172:175], v[196:199], v[80:83]
	v_mfma_f32_16x16x32_bf16 v[68:71], v[164:167], v[204:207], v[68:71]
	v_mfma_f32_16x16x32_bf16 v[64:67], v[172:175], v[204:207], v[64:67]
	s_setprio 0
	s_barrier
	s_mov_b64 s[50:51], s[66:67]
	v_mov_b32_e32 v152, v154
	s_add_i32 s54, s82, s52
	ds_read_b128 v[176:179], v163 offset:16384
	ds_read_b128 v[180:183], v163 offset:17408
	ds_read_b128 v[184:187], v163 offset:18432
	ds_read_b128 v[188:191], v163 offset:19456
	ds_read_b128 v[192:195], v163 offset:20480
	ds_read_b128 v[196:199], v163 offset:21504
	ds_read_b128 v[200:203], v163 offset:22528
	ds_read_b128 v[204:207], v163 offset:23552
	s_mov_b32 m0, s54
	s_nop 0
	global_load_lds_dwordx4 v152, s[50:51]
	v_mov_b32_e32 v152, v157
	s_add_i32 m0, s54, 0x2000
	s_nop 0
	global_load_lds_dwordx4 v152, s[50:51]
	s_add_u32 s50, s66, 0x80000
	s_addc_u32 s51, s67, 0
	v_mov_b32_e32 v152, v154
	s_add_i32 s54, s83, s52
	s_mov_b32 m0, s54
	s_nop 0
	global_load_lds_dwordx4 v152, s[50:51]
	v_mov_b32_e32 v152, v157
	s_add_i32 m0, s54, 0x2000
	s_nop 0
	global_load_lds_dwordx4 v152, s[50:51]
	s_mov_b64 s[50:51], s[68:69]
	v_mov_b32_e32 v152, v155
	s_mov_b32 m0, s49
	s_nop 0
	global_load_lds_dwordx4 v152, s[50:51]
	v_mov_b32_e32 v152, v158
	s_mov_b32 m0, s73
	s_nop 0
	global_load_lds_dwordx4 v152, s[50:51]
	s_waitcnt vmcnt(8)
	s_waitcnt lgkmcnt(0)
	s_barrier
	s_setprio 1
	s_waitcnt lgkmcnt(0)
	v_mfma_f32_16x16x32_bf16 v[60:63], v[96:99], v[176:179], v[60:63]
	v_mfma_f32_16x16x32_bf16 v[56:59], v[104:107], v[176:179], v[56:59]
	v_mfma_f32_16x16x32_bf16 v[44:47], v[96:99], v[184:187], v[44:47]
	v_mfma_f32_16x16x32_bf16 v[40:43], v[104:107], v[184:187], v[40:43]
	v_mfma_f32_16x16x32_bf16 v[20:23], v[96:99], v[192:195], v[20:23]
	v_mfma_f32_16x16x32_bf16 v[16:19], v[104:107], v[192:195], v[16:19]
	v_mfma_f32_16x16x32_bf16 v[4:7], v[96:99], v[200:203], v[4:7]
	v_mfma_f32_16x16x32_bf16 v[0:3], v[104:107], v[200:203], v[0:3]
	v_mfma_f32_16x16x32_bf16 v[60:63], v[100:103], v[180:183], v[60:63]
	v_mfma_f32_16x16x32_bf16 v[56:59], v[108:111], v[180:183], v[56:59]
	v_mfma_f32_16x16x32_bf16 v[44:47], v[100:103], v[188:191], v[44:47]
	v_mfma_f32_16x16x32_bf16 v[40:43], v[108:111], v[188:191], v[40:43]
	v_mfma_f32_16x16x32_bf16 v[20:23], v[100:103], v[196:199], v[20:23]
	v_mfma_f32_16x16x32_bf16 v[16:19], v[108:111], v[196:199], v[16:19]
	v_mfma_f32_16x16x32_bf16 v[4:7], v[100:103], v[204:207], v[4:7]
	v_mfma_f32_16x16x32_bf16 v[0:3], v[108:111], v[204:207], v[0:3]
	s_setprio 0
	s_setprio 1
	v_mfma_f32_16x16x32_bf16 v[52:55], v[148:151], v[176:179], v[52:55]
	v_mfma_f32_16x16x32_bf16 v[48:51], v[168:171], v[176:179], v[48:51]
	v_mfma_f32_16x16x32_bf16 v[36:39], v[148:151], v[184:187], v[36:39]
	v_mfma_f32_16x16x32_bf16 v[32:35], v[168:171], v[184:187], v[32:35]
	v_mfma_f32_16x16x32_bf16 v[24:27], v[148:151], v[192:195], v[24:27]
	v_mfma_f32_16x16x32_bf16 v[28:31], v[168:171], v[192:195], v[28:31]
	v_mfma_f32_16x16x32_bf16 v[8:11], v[148:151], v[200:203], v[8:11]
	v_mfma_f32_16x16x32_bf16 v[12:15], v[168:171], v[200:203], v[12:15]
	v_mfma_f32_16x16x32_bf16 v[52:55], v[164:167], v[180:183], v[52:55]
	v_mfma_f32_16x16x32_bf16 v[48:51], v[172:175], v[180:183], v[48:51]
	v_mfma_f32_16x16x32_bf16 v[36:39], v[164:167], v[188:191], v[36:39]
	v_mfma_f32_16x16x32_bf16 v[32:35], v[172:175], v[188:191], v[32:35]
	v_mfma_f32_16x16x32_bf16 v[24:27], v[164:167], v[196:199], v[24:27]
	v_mfma_f32_16x16x32_bf16 v[28:31], v[172:175], v[196:199], v[28:31]
	v_mfma_f32_16x16x32_bf16 v[8:11], v[164:167], v[204:207], v[8:11]
	v_mfma_f32_16x16x32_bf16 v[12:15], v[172:175], v[204:207], v[12:15]
	s_setprio 0
	s_barrier
; #define PG8_STAGE(bufoff, gbase, voff) do { const char* _gb = (const char*)(gbase); asm volatile("" : "+s"(_gb)); _Pragma("unroll") for (int _i = 0; _i < 2; ++_i) { unsigned _vo = (voff)[_i]; asm volatile("" : "+v"(_vo)); \
;         __builtin_amdgcn_global_load_lds((const unsigned*)(_gb + _vo), (LAS unsigned*)(lds + (bufoff) + ldsw + _i * 8192), 16, 0, 0); } } while (0)
; #define PG8_WAIT_V(n) asm volatile("s_waitcnt vmcnt(" #n ")" ::: "memory")
; #define PG8_WAIT_L(n) asm volatile("s_waitcnt lgkmcnt(" #n ")" ::: "memory")
; #define PG8_BAR __builtin_amdgcn_s_barrier()
; #define PG8_SCHED __builtin_amdgcn_sched_barrier(0)
; template <class Epi, class Sched, bool ALIGN_EPI, bool GATHER, bool F8 = false>
; __device__ __forceinline__ void gemm_phase(LAS unsigned char* lds, const Gemm g, const Sched& S, const Epi& E, const LAS int* gtok, const int tid) {
;     ...
;             PG8_LDB(B0, 1, 0); PG8_LDB(B1, 1, 1); PG8_SCHED; PG8_LDA(At, 1, 0); PG8_STAGE(PG8_SA(0, 1), a2, vS[1]);
;             PG8_WAIT_V(8); PG8_WAIT_L(0); PG8_BAR; PG8_MMA(0, 0, At, B0); PG8_MMA(0, 1, At, B1); PG8_BAR; PG8_SCHED;
;             PG8_LDA(At, 1, 1); PG8_STAGE(PG8_SB(1, 0), b3, voffB); PG8_STAGE(PG8_SB(1, 1), b3 + hstep, voffB); PG8_STAGE(PG8_SA(1, 0), a3, vS[0]);
;             PG8_WAIT_V(8); PG8_WAIT_L(0); PG8_BAR; PG8_MMA(1, 0, At, B0); PG8_MMA(1, 1, At, B1); PG8_BAR; PG8_SCHED;
;         }
	s_add_i32 s54, 0, 0x18000
	s_add_i32 s55, 0, 0x1c000
	v_add_u32_e32 v108, s54, v160
	v_add_u32_e32 v152, s55, v160
	ds_read_b128 v[96:99], v108
	ds_read_b128 v[100:103], v108 offset:1024
	ds_read_b128 v[104:107], v108 offset:2048
	ds_read_b128 v[108:111], v108 offset:3072
	ds_read_b128 v[148:151], v152
	ds_read_b128 v[164:167], v152 offset:1024
	ds_read_b128 v[168:171], v152 offset:2048
	ds_read_b128 v[172:175], v152 offset:3072
	v_mov_b32_e32 v152, v156
	s_mov_b32 m0, s74
	ds_read_b128 v[176:179], v163 offset:32768
	ds_read_b128 v[180:183], v163 offset:33792
	ds_read_b128 v[184:187], v163 offset:34816
	ds_read_b128 v[188:191], v163 offset:35840
	ds_read_b128 v[192:195], v163 offset:36864
	ds_read_b128 v[196:199], v163 offset:37888
	ds_read_b128 v[200:203], v163 offset:38912
	ds_read_b128 v[204:207], v163 offset:39936
	s_nop 0
	global_load_lds_dwordx4 v152, s[68:69]
	v_mov_b32_e32 v152, v159
	s_mov_b32 m0, s75
	s_nop 0
	global_load_lds_dwordx4 v152, s[68:69]
	s_waitcnt vmcnt(8)
	s_waitcnt lgkmcnt(0)
	s_barrier
	s_setprio 1
	s_waitcnt lgkmcnt(0)
	v_mfma_f32_16x16x32_bf16 v[140:143], v[96:99], v[176:179], v[140:143]
	v_mfma_f32_16x16x32_bf16 v[136:139], v[104:107], v[176:179], v[136:139]
	v_mfma_f32_16x16x32_bf16 v[124:127], v[96:99], v[184:187], v[124:127]
	v_mfma_f32_16x16x32_bf16 v[120:123], v[104:107], v[184:187], v[120:123]
	v_mfma_f32_16x16x32_bf16 v[92:95], v[96:99], v[192:195], v[92:95]
	v_mfma_f32_16x16x32_bf16 v[88:91], v[104:107], v[192:195], v[88:91]
	v_mfma_f32_16x16x32_bf16 v[76:79], v[96:99], v[200:203], v[76:79]
	v_mfma_f32_16x16x32_bf16 v[72:75], v[104:107], v[200:203], v[72:75]
	v_mfma_f32_16x16x32_bf16 v[140:143], v[100:103], v[180:183], v[140:143]
	v_mfma_f32_16x16x32_bf16 v[136:139], v[108:111], v[180:183], v[136:139]
	v_mfma_f32_16x16x32_bf16 v[124:127], v[100:103], v[188:191], v[124:127]
	v_mfma_f32_16x16x32_bf16 v[120:123], v[108:111], v[188:191], v[120:123]
	v_mfma_f32_16x16x32_bf16 v[92:95], v[100:103], v[196:199], v[92:95]
	v_mfma_f32_16x16x32_bf16 v[88:91], v[108:111], v[196:199], v[88:91]
	v_mfma_f32_16x16x32_bf16 v[76:79], v[100:103], v[204:207], v[76:79]
	v_mfma_f32_16x16x32_bf16 v[72:75], v[108:111], v[204:207], v[72:75]
	s_setprio 0
	s_setprio 1
	v_mfma_f32_16x16x32_bf16 v[132:135], v[148:151], v[176:179], v[132:135]
	v_mfma_f32_16x16x32_bf16 v[128:131], v[168:171], v[176:179], v[128:131]
	v_mfma_f32_16x16x32_bf16 v[116:119], v[148:151], v[184:187], v[116:119]
	v_mfma_f32_16x16x32_bf16 v[112:115], v[168:171], v[184:187], v[112:115]
	v_mfma_f32_16x16x32_bf16 v[84:87], v[148:151], v[192:195], v[84:87]
	v_mfma_f32_16x16x32_bf16 v[80:83], v[168:171], v[192:195], v[80:83]
	v_mfma_f32_16x16x32_bf16 v[68:71], v[148:151], v[200:203], v[68:71]
	v_mfma_f32_16x16x32_bf16 v[64:67], v[168:171], v[200:203], v[64:67]
	v_mfma_f32_16x16x32_bf16 v[132:135], v[164:167], v[180:183], v[132:135]
	v_mfma_f32_16x16x32_bf16 v[128:131], v[172:175], v[180:183], v[128:131]
	v_mfma_f32_16x16x32_bf16 v[116:119], v[164:167], v[188:191], v[116:119]
	v_mfma_f32_16x16x32_bf16 v[112:115], v[172:175], v[188:191], v[112:115]
	v_mfma_f32_16x16x32_bf16 v[84:87], v[164:167], v[196:199], v[84:87]
	v_mfma_f32_16x16x32_bf16 v[80:83], v[172:175], v[196:199], v[80:83]
	v_mfma_f32_16x16x32_bf16 v[68:71], v[164:167], v[204:207], v[68:71]
	v_mfma_f32_16x16x32_bf16 v[64:67], v[172:175], v[204:207], v[64:67]
	s_setprio 0
	s_barrier
	s_add_u32 s50, s66, 0x80
	s_addc_u32 s51, s67, 0
	v_mov_b32_e32 v152, v154
	s_add_i32 s54, s54, s52
	ds_read_b128 v[176:179], v163 offset:49152
	ds_read_b128 v[180:183], v163 offset:50176
	ds_read_b128 v[184:187], v163 offset:51200
	ds_read_b128 v[188:191], v163 offset:52224
	ds_read_b128 v[192:195], v163 offset:53248
	ds_read_b128 v[196:199], v163 offset:54272
	ds_read_b128 v[200:203], v163 offset:55296
	ds_read_b128 v[204:207], v163 offset:56320
	s_mov_b32 m0, s54
	s_nop 0
	global_load_lds_dwordx4 v152, s[50:51]
	v_mov_b32_e32 v152, v157
	s_add_i32 m0, s54, 0x2000
	s_nop 0
	global_load_lds_dwordx4 v152, s[50:51]
	s_add_u32 s50, s66, 0x80080
	s_addc_u32 s51, s67, 0
	v_mov_b32_e32 v152, v154
	s_add_i32 s54, s55, s52
	s_mov_b32 m0, s54
	s_nop 0
	global_load_lds_dwordx4 v152, s[50:51]
	v_mov_b32_e32 v152, v157
	s_add_i32 m0, s54, 0x2000
	s_nop 0
	global_load_lds_dwordx4 v152, s[50:51]
	v_mov_b32_e32 v152, v155
	s_mov_b32 m0, s79
	s_nop 0
	global_load_lds_dwordx4 v152, s[64:65]
	v_mov_b32_e32 v152, v158
	s_mov_b32 m0, s80
	s_nop 0
	global_load_lds_dwordx4 v152, s[64:65]
	s_waitcnt vmcnt(8)
	s_waitcnt lgkmcnt(0)
	s_barrier
	s_setprio 1
	s_waitcnt lgkmcnt(0)
	v_mfma_f32_16x16x32_bf16 v[60:63], v[96:99], v[176:179], v[60:63]
	v_mfma_f32_16x16x32_bf16 v[56:59], v[104:107], v[176:179], v[56:59]
	v_mfma_f32_16x16x32_bf16 v[44:47], v[96:99], v[184:187], v[44:47]
	v_mfma_f32_16x16x32_bf16 v[40:43], v[104:107], v[184:187], v[40:43]
	v_mfma_f32_16x16x32_bf16 v[20:23], v[96:99], v[192:195], v[20:23]
	v_mfma_f32_16x16x32_bf16 v[16:19], v[104:107], v[192:195], v[16:19]
	v_mfma_f32_16x16x32_bf16 v[4:7], v[96:99], v[200:203], v[4:7]
	v_mfma_f32_16x16x32_bf16 v[0:3], v[104:107], v[200:203], v[0:3]
	v_mfma_f32_16x16x32_bf16 v[60:63], v[100:103], v[180:183], v[60:63]
	v_mfma_f32_16x16x32_bf16 v[56:59], v[108:111], v[180:183], v[56:59]
	v_mfma_f32_16x16x32_bf16 v[44:47], v[100:103], v[188:191], v[44:47]
	v_mfma_f32_16x16x32_bf16 v[40:43], v[108:111], v[188:191], v[40:43]
	v_mfma_f32_16x16x32_bf16 v[20:23], v[100:103], v[196:199], v[20:23]
	v_mfma_f32_16x16x32_bf16 v[16:19], v[108:111], v[196:199], v[16:19]
	v_mfma_f32_16x16x32_bf16 v[4:7], v[100:103], v[204:207], v[4:7]
	v_mfma_f32_16x16x32_bf16 v[0:3], v[108:111], v[204:207], v[0:3]
	s_setprio 0
	s_setprio 1
	v_mfma_f32_16x16x32_bf16 v[52:55], v[148:151], v[176:179], v[52:55]
	v_mfma_f32_16x16x32_bf16 v[48:51], v[168:171], v[176:179], v[48:51]
	v_mfma_f32_16x16x32_bf16 v[36:39], v[148:151], v[184:187], v[36:39]
	v_mfma_f32_16x16x32_bf16 v[32:35], v[168:171], v[184:187], v[32:35]
	v_mfma_f32_16x16x32_bf16 v[24:27], v[148:151], v[192:195], v[24:27]
	v_mfma_f32_16x16x32_bf16 v[28:31], v[168:171], v[192:195], v[28:31]
	v_mfma_f32_16x16x32_bf16 v[8:11], v[148:151], v[200:203], v[8:11]
	v_mfma_f32_16x16x32_bf16 v[12:15], v[168:171], v[200:203], v[12:15]
	v_mfma_f32_16x16x32_bf16 v[52:55], v[164:167], v[180:183], v[52:55]
	v_mfma_f32_16x16x32_bf16 v[48:51], v[172:175], v[180:183], v[48:51]
	v_mfma_f32_16x16x32_bf16 v[36:39], v[164:167], v[188:191], v[36:39]
	v_mfma_f32_16x16x32_bf16 v[32:35], v[172:175], v[188:191], v[32:35]
	v_mfma_f32_16x16x32_bf16 v[24:27], v[164:167], v[196:199], v[24:27]
	v_mfma_f32_16x16x32_bf16 v[28:31], v[172:175], v[196:199], v[28:31]
	v_mfma_f32_16x16x32_bf16 v[8:11], v[164:167], v[204:207], v[8:11]
	v_mfma_f32_16x16x32_bf16 v[12:15], v[172:175], v[204:207], v[12:15]
	s_setprio 0
	s_barrier
	s_add_i32 s88, s88, 2
	s_add_u32 s87, s87, 0x100
	s_addc_u32 s33, s33, 0
	s_cmp_gt_u32 s88, 29
	s_mov_b64 s[50:51], s[62:63]
	s_cbranch_scc0 .LBB0_486
	s_and_b64 vcc, exec, s[6:7]
	s_cbranch_vccz .LBB0_489
	s_barrier
; __device__ __forceinline__ unsigned cvt_pk_bf16(float lo, float hi) { unsigned r; asm volatile("v_cvt_pk_bf16_f32 %0, %1, %2" : "=v"(r) : "v"(lo), "v"(hi)); return r; }
; __device__ __forceinline__ unsigned pk4_fp8(float a, float b, float c, float d) { int p = 0; p = __builtin_amdgcn_cvt_pk_fp8_f32(a, b, p, false); p = __builtin_amdgcn_cvt_pk_fp8_f32(c, d, p, true); return (unsigned)p; }
;     __device__ __forceinline__ void operator()(AccRef acc, const Unit& u, int wr, int wc, int fr, int fq) const {
;         const int row0 = u.pm * BM + wr * 64 + fr, col0 = u.pn * BM + wc * 32 + 8 * fq;
;         f32x4 gv[2][2];
; #pragma unroll
;         for (int bj = 0; bj < 2; ++bj)
; #pragma unroll
;             for (int n = 0; n < 2; ++n) gv[bj][n] = *(const f32x4*)(g2 + col0 + bj * HALF + 4 * n);
; #pragma unroll
;         for (int ai = 0; ai < 2; ++ai)
; #pragma unroll
;             for (int m = 0; m < 4; ++m) { const size_t ro = (size_t)(row0 + ai * HALF + m * 16) * DM + col0;
;                 f32x4 xv[2][2];
; #pragma unroll
;                 for (int bj = 0; bj < 2; ++bj)
; #pragma unroll
;                     for (int n = 0; n < 2; ++n) xv[bj][n] = __builtin_nontemporal_load((const f32x4*)(X + ro + bj * HALF + 4 * n));
; #pragma unroll
;                 for (int bj = 0; bj < 2; ++bj) { const f32x4 a = xv[bj][0] + acc[ai][bj][m][0], b = xv[bj][1] + acc[ai][bj][m][1];
;                     { v4u xo; xo.x = cvt_pk_bf16(a[0], a[1]); xo.y = cvt_pk_bf16(a[2], a[3]); xo.z = cvt_pk_bf16(b[0], b[1]); xo.w = cvt_pk_bf16(b[2], b[3]); *(v4u*)(O + ro + bj * HALF) = xo; }
;                     const f32x4 ha = a * gv[bj][0], hb = b * gv[bj][1];
;                     v2u w; w.x = pk4_fp8(ha[0], ha[1], ha[2], ha[3]); w.y = pk4_fp8(hb[0], hb[1], hb[2], hb[3]);
;                     *(v2u*)((unsigned char*)HN + ro + bj * HALF) = w; } }
.LBB0_489:
	s_lshl_b32 s33, s48, 8
	v_mbcnt_lo_u32_b32 v96, -1, 0
	v_mbcnt_hi_u32_b32 v96, -1, v96
	s_add_i32 s33, s33, s77
	s_lshl_b32 s41, s84, 8
	v_ashrrev_i32_e32 v97, 1, v96
	s_or_b32 s41, s41, s78
	v_and_b32_e32 v97, -8, v97
	v_and_or_b32 v152, v96, 15, s33
	v_add_u32_e32 v150, s41, v97
	v_ashrrev_i32_e32 v153, 31, v152
	v_ashrrev_i32_e32 v151, 31, v150
	v_lshlrev_b64 v[96:97], 11, v[152:153]
	v_lshl_add_u64 v[148:149], v[96:97], 0, v[150:151]
	v_lshl_add_u64 v[96:97], v[148:149], 2, s[36:37]
	global_load_dwordx4 v[164:167], v[96:97], off nt
	global_load_dwordx4 v[168:171], v[96:97], off offset:16 nt
	global_load_dwordx4 v[172:175], v[96:97], off offset:512 nt
	global_load_dwordx4 v[176:179], v[96:97], off offset:528 nt
	v_lshl_add_u64 v[96:97], v[150:151], 2, s[10:11]
	global_load_dwordx4 v[108:111], v[96:97], off
	global_load_dwordx4 v[104:107], v[96:97], off offset:16
	global_load_dwordx4 v[100:103], v[96:97], off offset:512
	s_nop 0
	global_load_dwordx4 v[96:99], v[96:97], off offset:528
	v_mov_b32_e32 v180, 0
	v_mov_b32_e32 v181, 0
	v_mov_b32_e32 v182, 0
	v_mov_b32_e32 v183, 0
	v_or_b32_e32 v184, 16, v152
	v_ashrrev_i32_e32 v185, 31, v184
	v_lshlrev_b64 v[184:185], 11, v[184:185]
	v_lshl_add_u64 v[186:187], v[148:149], 1, s[38:39]
	v_lshl_add_u64 v[188:189], s[60:61], 0, v[148:149]
	v_lshl_add_u64 v[184:185], v[184:185], 0, v[150:151]
	v_lshl_add_u64 v[190:191], v[184:185], 2, s[36:37]
	s_andn2_b64 vcc, exec, s[0:1]
	s_mov_b64 s[0:1], -1
	s_waitcnt vmcnt(0)
	v_pk_add_f32 v[140:141], v[140:141], v[164:165]
	v_pk_add_f32 v[136:137], v[136:137], v[168:169]
	v_pk_add_f32 v[142:143], v[142:143], v[166:167]
	v_pk_add_f32 v[164:165], v[130:131], v[178:179]
	v_pk_add_f32 v[166:167], v[128:129], v[176:177]
	v_cvt_pk_bf16_f32 v128, v140, v141
	v_cvt_pk_bf16_f32 v129, v142, v143
	v_cvt_pk_bf16_f32 v130, v136, v137
	v_pk_mul_f32 v[140:141], v[108:109], v[140:141]
	v_pk_mul_f32 v[136:137], v[104:105], v[136:137]
	v_pk_add_f32 v[132:133], v[132:133], v[172:173]
	v_cvt_pk_fp8_f32 v180, v140, v141
	v_cvt_pk_fp8_f32 v181, v136, v137
	v_pk_add_f32 v[138:139], v[138:139], v[170:171]
	v_pk_add_f32 v[134:135], v[134:135], v[174:175]
	v_pk_mul_f32 v[170:171], v[100:101], v[132:133]
	v_pk_mul_f32 v[174:175], v[96:97], v[166:167]
	v_cvt_pk_fp8_f32 v182, v170, v171
	v_cvt_pk_fp8_f32 v183, v174, v175
	v_cvt_pk_bf16_f32 v131, v138, v139
	v_pk_mul_f32 v[142:143], v[110:111], v[142:143]
	v_pk_mul_f32 v[138:139], v[106:107], v[138:139]
	v_cvt_pk_fp8_f32 v180, v142, v143 op_sel:[0,0,1]
	v_cvt_pk_fp8_f32 v181, v138, v139 op_sel:[0,0,1]
	v_pk_mul_f32 v[168:169], v[102:103], v[134:135]
	v_pk_mul_f32 v[172:173], v[98:99], v[164:165]
	v_cvt_pk_fp8_f32 v182, v168, v169 op_sel:[0,0,1]
	v_cvt_pk_fp8_f32 v183, v172, v173 op_sel:[0,0,1]
	global_store_dwordx4 v[186:187], v[128:131], off
	global_store_dwordx2 v[188:189], v[180:181], off
	v_or_b32_e32 v168, 32, v152
	v_cvt_pk_bf16_f32 v128, v132, v133
	v_cvt_pk_bf16_f32 v129, v134, v135
	v_cvt_pk_bf16_f32 v130, v166, v167
	v_cvt_pk_bf16_f32 v131, v164, v165
	global_store_dwordx4 v[186:187], v[128:131], off offset:256
	global_store_dwordx2 v[188:189], v[182:183], off offset:128
	global_load_dwordx4 v[128:131], v[190:191], off nt
	s_nop 0
	global_load_dwordx4 v[132:135], v[190:191], off offset:16 nt
	global_load_dwordx4 v[136:139], v[190:191], off offset:512 nt
	global_load_dwordx4 v[140:143], v[190:191], off offset:528 nt
	v_mov_b32_e32 v164, 0
	v_mov_b32_e32 v165, 0
	v_mov_b32_e32 v166, 0
	v_mov_b32_e32 v167, 0
	v_ashrrev_i32_e32 v169, 31, v168
	v_lshlrev_b64 v[168:169], 11, v[168:169]
	v_lshl_add_u64 v[170:171], v[184:185], 1, s[38:39]
	v_lshl_add_u64 v[172:173], s[60:61], 0, v[184:185]
	v_lshl_add_u64 v[168:169], v[168:169], 0, v[150:151]
	v_lshl_add_u64 v[174:175], v[168:169], 2, s[36:37]
	s_waitcnt vmcnt(3)
	v_pk_add_f32 v[124:125], v[124:125], v[128:129]
	s_waitcnt vmcnt(2)
	v_pk_add_f32 v[120:121], v[120:121], v[132:133]
	v_pk_add_f32 v[126:127], v[126:127], v[130:131]
	s_waitcnt vmcnt(0)
	v_pk_add_f32 v[128:129], v[114:115], v[142:143]
	v_pk_add_f32 v[130:131], v[112:113], v[140:141]
	v_cvt_pk_bf16_f32 v112, v124, v125
	v_cvt_pk_bf16_f32 v113, v126, v127
	v_cvt_pk_bf16_f32 v114, v120, v121
	v_pk_mul_f32 v[124:125], v[108:109], v[124:125]
	v_pk_mul_f32 v[120:121], v[104:105], v[120:121]
	v_pk_add_f32 v[116:117], v[116:117], v[136:137]
	v_cvt_pk_fp8_f32 v164, v124, v125
	v_cvt_pk_fp8_f32 v165, v120, v121
	v_pk_add_f32 v[122:123], v[122:123], v[134:135]
	v_pk_add_f32 v[118:119], v[118:119], v[138:139]
	v_pk_mul_f32 v[134:135], v[100:101], v[116:117]
	v_pk_mul_f32 v[138:139], v[96:97], v[130:131]
	v_cvt_pk_fp8_f32 v166, v134, v135
	v_cvt_pk_fp8_f32 v167, v138, v139
	v_cvt_pk_bf16_f32 v115, v122, v123
	v_pk_mul_f32 v[126:127], v[110:111], v[126:127]
	v_pk_mul_f32 v[122:123], v[106:107], v[122:123]
	v_cvt_pk_fp8_f32 v164, v126, v127 op_sel:[0,0,1]
	v_cvt_pk_fp8_f32 v165, v122, v123 op_sel:[0,0,1]
	v_pk_mul_f32 v[132:133], v[102:103], v[118:119]
	v_pk_mul_f32 v[136:137], v[98:99], v[128:129]
	v_cvt_pk_fp8_f32 v166, v132, v133 op_sel:[0,0,1]
	v_cvt_pk_fp8_f32 v167, v136, v137 op_sel:[0,0,1]
	global_store_dwordx4 v[170:171], v[112:115], off
	global_store_dwordx2 v[172:173], v[164:165], off
	v_or_b32_e32 v132, 48, v152
	v_cvt_pk_bf16_f32 v112, v116, v117
	v_cvt_pk_bf16_f32 v113, v118, v119
	v_cvt_pk_bf16_f32 v114, v130, v131
	v_cvt_pk_bf16_f32 v115, v128, v129
	global_store_dwordx4 v[170:171], v[112:115], off offset:256
	global_store_dwordx2 v[172:173], v[166:167], off offset:128
	global_load_dwordx4 v[112:115], v[174:175], off nt
	s_nop 0
	global_load_dwordx4 v[116:119], v[174:175], off offset:16 nt
	global_load_dwordx4 v[120:123], v[174:175], off offset:512 nt
	global_load_dwordx4 v[124:127], v[174:175], off offset:528 nt
	v_mov_b32_e32 v128, 0
	v_mov_b32_e32 v129, 0
	v_mov_b32_e32 v130, 0
	v_mov_b32_e32 v131, 0
	v_ashrrev_i32_e32 v133, 31, v132
	v_lshlrev_b64 v[132:133], 11, v[132:133]
	v_lshl_add_u64 v[134:135], v[168:169], 1, s[38:39]
	v_lshl_add_u64 v[136:137], s[60:61], 0, v[168:169]
	v_lshl_add_u64 v[132:133], v[132:133], 0, v[150:151]
	v_lshl_add_u64 v[138:139], v[132:133], 2, s[36:37]
	s_waitcnt vmcnt(3)
; __device__ __forceinline__ unsigned cvt_pk_bf16(float lo, float hi) { unsigned r; asm volatile("v_cvt_pk_bf16_f32 %0, %1, %2" : "=v"(r) : "v"(lo), "v"(hi)); return r; }
; __device__ __forceinline__ unsigned pk4_fp8(float a, float b, float c, float d) { int p = 0; p = __builtin_amdgcn_cvt_pk_fp8_f32(a, b, p, false); p = __builtin_amdgcn_cvt_pk_fp8_f32(c, d, p, true); return (unsigned)p; }
;     __device__ __forceinline__ void operator()(AccRef acc, const Unit& u, int wr, int wc, int fr, int fq) const {
;     ...
;         for (int ai = 0; ai < 2; ++ai)
; #pragma unroll
;             for (int m = 0; m < 4; ++m) { const size_t ro = (size_t)(row0 + ai * HALF + m * 16) * DM + col0;
;                 f32x4 xv[2][2];
; #pragma unroll
;                 for (int bj = 0; bj < 2; ++bj)
; #pragma unroll
;                     for (int n = 0; n < 2; ++n) xv[bj][n] = __builtin_nontemporal_load((const f32x4*)(X + ro + bj * HALF + 4 * n));
; #pragma unroll
;                 for (int bj = 0; bj < 2; ++bj) { const f32x4 a = xv[bj][0] + acc[ai][bj][m][0], b = xv[bj][1] + acc[ai][bj][m][1];
;                     { v4u xo; xo.x = cvt_pk_bf16(a[0], a[1]); xo.y = cvt_pk_bf16(a[2], a[3]); xo.z = cvt_pk_bf16(b[0], b[1]); xo.w = cvt_pk_bf16(b[2], b[3]); *(v4u*)(O + ro + bj * HALF) = xo; }
;                     const f32x4 ha = a * gv[bj][0], hb = b * gv[bj][1];
;                     v2u w; w.x = pk4_fp8(ha[0], ha[1], ha[2], ha[3]); w.y = pk4_fp8(hb[0], hb[1], hb[2], hb[3]);
;                     *(v2u*)((unsigned char*)HN + ro + bj * HALF) = w; } }
	v_pk_add_f32 v[92:93], v[92:93], v[112:113]
	s_waitcnt vmcnt(2)
	v_pk_add_f32 v[88:89], v[88:89], v[116:117]
	v_pk_add_f32 v[94:95], v[94:95], v[114:115]
	s_waitcnt vmcnt(0)
	v_pk_add_f32 v[112:113], v[82:83], v[126:127]
	v_pk_add_f32 v[114:115], v[80:81], v[124:125]
	v_cvt_pk_bf16_f32 v80, v92, v93
	v_cvt_pk_bf16_f32 v81, v94, v95
	v_cvt_pk_bf16_f32 v82, v88, v89
	v_pk_mul_f32 v[92:93], v[108:109], v[92:93]
	v_pk_mul_f32 v[88:89], v[104:105], v[88:89]
	v_pk_add_f32 v[84:85], v[84:85], v[120:121]
	v_cvt_pk_fp8_f32 v128, v92, v93
	v_cvt_pk_fp8_f32 v129, v88, v89
	v_pk_add_f32 v[90:91], v[90:91], v[118:119]
	v_pk_add_f32 v[86:87], v[86:87], v[122:123]
	v_pk_mul_f32 v[118:119], v[100:101], v[84:85]
	v_pk_mul_f32 v[122:123], v[96:97], v[114:115]
	v_cvt_pk_fp8_f32 v130, v118, v119
	v_cvt_pk_fp8_f32 v131, v122, v123
	v_cvt_pk_bf16_f32 v83, v90, v91
	v_pk_mul_f32 v[94:95], v[110:111], v[94:95]
	v_pk_mul_f32 v[90:91], v[106:107], v[90:91]
	v_cvt_pk_fp8_f32 v128, v94, v95 op_sel:[0,0,1]
	v_cvt_pk_fp8_f32 v129, v90, v91 op_sel:[0,0,1]
	v_pk_mul_f32 v[116:117], v[102:103], v[86:87]
	v_pk_mul_f32 v[120:121], v[98:99], v[112:113]
	v_cvt_pk_fp8_f32 v130, v116, v117 op_sel:[0,0,1]
	v_cvt_pk_fp8_f32 v131, v120, v121 op_sel:[0,0,1]
	global_store_dwordx4 v[134:135], v[80:83], off
	global_store_dwordx2 v[136:137], v[128:129], off
	v_lshl_add_u64 v[118:119], v[132:133], 1, s[38:39]
	v_cvt_pk_bf16_f32 v80, v84, v85
	v_cvt_pk_bf16_f32 v81, v86, v87
	v_cvt_pk_bf16_f32 v82, v114, v115
	v_cvt_pk_bf16_f32 v83, v112, v113
	global_store_dwordx4 v[134:135], v[80:83], off offset:256
	global_store_dwordx2 v[136:137], v[130:131], off offset:128
	global_load_dwordx4 v[80:83], v[138:139], off nt
	s_nop 0
	global_load_dwordx4 v[84:87], v[138:139], off offset:16 nt
	global_load_dwordx4 v[88:91], v[138:139], off offset:512 nt
	global_load_dwordx4 v[92:95], v[138:139], off offset:528 nt
	v_mov_b32_e32 v112, 0
	v_mov_b32_e32 v113, 0
	v_mov_b32_e32 v114, 0
	v_mov_b32_e32 v115, 0
	v_lshl_add_u64 v[120:121], s[60:61], 0, v[132:133]
	v_lshl_add_u64 v[116:117], v[148:149], 0, s[12:13]
	v_lshl_add_u64 v[122:123], v[116:117], 2, s[36:37]
	s_waitcnt vmcnt(3)
	v_pk_add_f32 v[76:77], v[76:77], v[80:81]
	s_waitcnt vmcnt(2)
	v_pk_add_f32 v[72:73], v[72:73], v[84:85]
	v_pk_add_f32 v[78:79], v[78:79], v[82:83]
	s_waitcnt vmcnt(0)
	v_pk_add_f32 v[80:81], v[66:67], v[94:95]
	v_pk_add_f32 v[82:83], v[64:65], v[92:93]
	v_cvt_pk_bf16_f32 v64, v76, v77
	v_cvt_pk_bf16_f32 v65, v78, v79
	v_cvt_pk_bf16_f32 v66, v72, v73
	v_pk_mul_f32 v[76:77], v[108:109], v[76:77]
	v_pk_mul_f32 v[72:73], v[104:105], v[72:73]
	v_pk_add_f32 v[68:69], v[68:69], v[88:89]
	v_cvt_pk_fp8_f32 v112, v76, v77
	v_cvt_pk_fp8_f32 v113, v72, v73
	v_pk_add_f32 v[74:75], v[74:75], v[86:87]
	v_pk_add_f32 v[70:71], v[70:71], v[90:91]
	v_pk_mul_f32 v[86:87], v[100:101], v[68:69]
	v_pk_mul_f32 v[90:91], v[96:97], v[82:83]
	v_cvt_pk_fp8_f32 v114, v86, v87
	v_cvt_pk_fp8_f32 v115, v90, v91
	v_cvt_pk_bf16_f32 v67, v74, v75
	v_pk_mul_f32 v[78:79], v[110:111], v[78:79]
	v_pk_mul_f32 v[74:75], v[106:107], v[74:75]
	v_cvt_pk_fp8_f32 v112, v78, v79 op_sel:[0,0,1]
	v_cvt_pk_fp8_f32 v113, v74, v75 op_sel:[0,0,1]
	v_pk_mul_f32 v[84:85], v[102:103], v[70:71]
	v_pk_mul_f32 v[88:89], v[98:99], v[80:81]
	v_cvt_pk_fp8_f32 v114, v84, v85 op_sel:[0,0,1]
	v_cvt_pk_fp8_f32 v115, v88, v89 op_sel:[0,0,1]
	global_store_dwordx4 v[118:119], v[64:67], off
	global_store_dwordx2 v[120:121], v[112:113], off
	v_lshl_add_u64 v[86:87], v[116:117], 1, s[38:39]
	v_cvt_pk_bf16_f32 v64, v68, v69
	v_cvt_pk_bf16_f32 v65, v70, v71
	v_cvt_pk_bf16_f32 v66, v82, v83
	v_cvt_pk_bf16_f32 v67, v80, v81
	global_store_dwordx4 v[118:119], v[64:67], off offset:256
	global_store_dwordx2 v[120:121], v[114:115], off offset:128
	global_load_dwordx4 v[64:67], v[122:123], off nt
	s_nop 0
	global_load_dwordx4 v[68:71], v[122:123], off offset:16 nt
	global_load_dwordx4 v[72:75], v[122:123], off offset:512 nt
	global_load_dwordx4 v[76:79], v[122:123], off offset:528 nt
	v_mov_b32_e32 v80, 0
	v_mov_b32_e32 v81, 0
	v_mov_b32_e32 v82, 0
	v_mov_b32_e32 v83, 0
	v_lshl_add_u64 v[88:89], s[60:61], 0, v[116:117]
	v_lshl_add_u64 v[84:85], v[148:149], 0, s[16:17]
	v_lshl_add_u64 v[90:91], v[84:85], 2, s[36:37]
	s_waitcnt vmcnt(3)
	v_pk_add_f32 v[60:61], v[60:61], v[64:65]
	s_waitcnt vmcnt(2)
	v_pk_add_f32 v[56:57], v[56:57], v[68:69]
	v_pk_add_f32 v[62:63], v[62:63], v[66:67]
	s_waitcnt vmcnt(0)
	v_pk_add_f32 v[64:65], v[50:51], v[78:79]
	v_pk_add_f32 v[66:67], v[48:49], v[76:77]
	v_cvt_pk_bf16_f32 v48, v60, v61
	v_cvt_pk_bf16_f32 v49, v62, v63
	v_cvt_pk_bf16_f32 v50, v56, v57
	v_pk_mul_f32 v[60:61], v[108:109], v[60:61]
	v_pk_mul_f32 v[56:57], v[104:105], v[56:57]
	v_pk_add_f32 v[52:53], v[52:53], v[72:73]
	v_cvt_pk_fp8_f32 v80, v60, v61
	v_cvt_pk_fp8_f32 v81, v56, v57
	v_pk_add_f32 v[58:59], v[58:59], v[70:71]
	v_pk_add_f32 v[54:55], v[54:55], v[74:75]
	v_pk_mul_f32 v[70:71], v[100:101], v[52:53]
	v_pk_mul_f32 v[74:75], v[96:97], v[66:67]
	v_cvt_pk_fp8_f32 v82, v70, v71
	v_cvt_pk_fp8_f32 v83, v74, v75
	v_cvt_pk_bf16_f32 v51, v58, v59
	v_pk_mul_f32 v[62:63], v[110:111], v[62:63]
	v_pk_mul_f32 v[58:59], v[106:107], v[58:59]
	v_cvt_pk_fp8_f32 v80, v62, v63 op_sel:[0,0,1]
	v_cvt_pk_fp8_f32 v81, v58, v59 op_sel:[0,0,1]
	v_pk_mul_f32 v[68:69], v[102:103], v[54:55]
	v_pk_mul_f32 v[72:73], v[98:99], v[64:65]
	v_cvt_pk_fp8_f32 v82, v68, v69 op_sel:[0,0,1]
	v_cvt_pk_fp8_f32 v83, v72, v73 op_sel:[0,0,1]
	global_store_dwordx4 v[86:87], v[48:51], off
	global_store_dwordx2 v[88:89], v[80:81], off
	v_lshl_add_u64 v[70:71], v[84:85], 1, s[38:39]
	v_cvt_pk_bf16_f32 v48, v52, v53
	v_cvt_pk_bf16_f32 v49, v54, v55
	v_cvt_pk_bf16_f32 v50, v66, v67
	v_cvt_pk_bf16_f32 v51, v64, v65
	global_store_dwordx4 v[86:87], v[48:51], off offset:256
	global_store_dwordx2 v[88:89], v[82:83], off offset:128
	global_load_dwordx4 v[48:51], v[90:91], off nt
	s_nop 0
	global_load_dwordx4 v[52:55], v[90:91], off offset:16 nt
	global_load_dwordx4 v[56:59], v[90:91], off offset:512 nt
	global_load_dwordx4 v[60:63], v[90:91], off offset:528 nt
	v_mov_b32_e32 v64, 0
	v_mov_b32_e32 v65, 0
	v_mov_b32_e32 v66, 0
	v_mov_b32_e32 v67, 0
	v_lshl_add_u64 v[72:73], s[60:61], 0, v[84:85]
	v_lshl_add_u64 v[68:69], v[148:149], 0, s[20:21]
	v_lshl_add_u64 v[74:75], v[68:69], 2, s[36:37]
	s_waitcnt vmcnt(3)
; __device__ __forceinline__ unsigned cvt_pk_bf16(float lo, float hi) { unsigned r; asm volatile("v_cvt_pk_bf16_f32 %0, %1, %2" : "=v"(r) : "v"(lo), "v"(hi)); return r; }
; __device__ __forceinline__ unsigned pk4_fp8(float a, float b, float c, float d) { int p = 0; p = __builtin_amdgcn_cvt_pk_fp8_f32(a, b, p, false); p = __builtin_amdgcn_cvt_pk_fp8_f32(c, d, p, true); return (unsigned)p; }
;     __device__ __forceinline__ void operator()(AccRef acc, const Unit& u, int wr, int wc, int fr, int fq) const {
;     ...
;         for (int ai = 0; ai < 2; ++ai)
; #pragma unroll
;             for (int m = 0; m < 4; ++m) { const size_t ro = (size_t)(row0 + ai * HALF + m * 16) * DM + col0;
;                 f32x4 xv[2][2];
; #pragma unroll
;                 for (int bj = 0; bj < 2; ++bj)
; #pragma unroll
;                     for (int n = 0; n < 2; ++n) xv[bj][n] = __builtin_nontemporal_load((const f32x4*)(X + ro + bj * HALF + 4 * n));
; #pragma unroll
;                 for (int bj = 0; bj < 2; ++bj) { const f32x4 a = xv[bj][0] + acc[ai][bj][m][0], b = xv[bj][1] + acc[ai][bj][m][1];
;                     { v4u xo; xo.x = cvt_pk_bf16(a[0], a[1]); xo.y = cvt_pk_bf16(a[2], a[3]); xo.z = cvt_pk_bf16(b[0], b[1]); xo.w = cvt_pk_bf16(b[2], b[3]); *(v4u*)(O + ro + bj * HALF) = xo; }
;                     const f32x4 ha = a * gv[bj][0], hb = b * gv[bj][1];
;                     v2u w; w.x = pk4_fp8(ha[0], ha[1], ha[2], ha[3]); w.y = pk4_fp8(hb[0], hb[1], hb[2], hb[3]);
;                     *(v2u*)((unsigned char*)HN + ro + bj * HALF) = w; } }
	v_pk_add_f32 v[44:45], v[44:45], v[48:49]
	s_waitcnt vmcnt(2)
	v_pk_add_f32 v[40:41], v[40:41], v[52:53]
	v_pk_add_f32 v[46:47], v[46:47], v[50:51]
	s_waitcnt vmcnt(0)
	v_pk_add_f32 v[48:49], v[34:35], v[62:63]
	v_pk_add_f32 v[50:51], v[32:33], v[60:61]
	v_cvt_pk_bf16_f32 v32, v44, v45
	v_cvt_pk_bf16_f32 v33, v46, v47
	v_cvt_pk_bf16_f32 v34, v40, v41
	v_pk_mul_f32 v[44:45], v[108:109], v[44:45]
	v_pk_mul_f32 v[40:41], v[104:105], v[40:41]
	v_pk_add_f32 v[36:37], v[36:37], v[56:57]
	v_cvt_pk_fp8_f32 v64, v44, v45
	v_cvt_pk_fp8_f32 v65, v40, v41
	v_pk_add_f32 v[42:43], v[42:43], v[54:55]
	v_pk_add_f32 v[38:39], v[38:39], v[58:59]
	v_pk_mul_f32 v[54:55], v[100:101], v[36:37]
	v_pk_mul_f32 v[58:59], v[96:97], v[50:51]
	v_cvt_pk_fp8_f32 v66, v54, v55
	v_cvt_pk_fp8_f32 v67, v58, v59
	v_cvt_pk_bf16_f32 v35, v42, v43
	v_pk_mul_f32 v[46:47], v[110:111], v[46:47]
	v_pk_mul_f32 v[42:43], v[106:107], v[42:43]
	v_cvt_pk_fp8_f32 v64, v46, v47 op_sel:[0,0,1]
	v_cvt_pk_fp8_f32 v65, v42, v43 op_sel:[0,0,1]
	v_pk_mul_f32 v[52:53], v[102:103], v[38:39]
	v_pk_mul_f32 v[56:57], v[98:99], v[48:49]
	v_cvt_pk_fp8_f32 v66, v52, v53 op_sel:[0,0,1]
	v_cvt_pk_fp8_f32 v67, v56, v57 op_sel:[0,0,1]
	global_store_dwordx4 v[70:71], v[32:35], off
	global_store_dwordx2 v[72:73], v[64:65], off
	v_lshl_add_u64 v[54:55], v[68:69], 1, s[38:39]
	v_cvt_pk_bf16_f32 v32, v36, v37
	v_cvt_pk_bf16_f32 v33, v38, v39
	v_cvt_pk_bf16_f32 v34, v50, v51
	v_cvt_pk_bf16_f32 v35, v48, v49
	global_store_dwordx4 v[70:71], v[32:35], off offset:256
	global_store_dwordx2 v[72:73], v[66:67], off offset:128
	global_load_dwordx4 v[32:35], v[74:75], off nt
	s_nop 0
	global_load_dwordx4 v[36:39], v[74:75], off offset:16 nt
	global_load_dwordx4 v[40:43], v[74:75], off offset:512 nt
	global_load_dwordx4 v[44:47], v[74:75], off offset:528 nt
	v_mov_b32_e32 v48, 0
	v_mov_b32_e32 v49, 0
	v_mov_b32_e32 v50, 0
	v_mov_b32_e32 v51, 0
	v_lshl_add_u64 v[56:57], s[60:61], 0, v[68:69]
	v_lshl_add_u64 v[52:53], v[148:149], 0, s[22:23]
	v_lshl_add_u64 v[58:59], v[52:53], 2, s[36:37]
	s_waitcnt vmcnt(3)
	v_pk_add_f32 v[22:23], v[22:23], v[34:35]
	v_pk_add_f32 v[20:21], v[20:21], v[32:33]
	s_waitcnt vmcnt(2)
	v_pk_add_f32 v[34:35], v[16:17], v[36:37]
	v_pk_add_f32 v[32:33], v[18:19], v[38:39]
	v_cvt_pk_bf16_f32 v16, v20, v21
	v_cvt_pk_bf16_f32 v17, v22, v23
	v_cvt_pk_bf16_f32 v18, v34, v35
	v_pk_mul_f32 v[20:21], v[108:109], v[20:21]
	v_pk_mul_f32 v[34:35], v[104:105], v[34:35]
	s_waitcnt vmcnt(1)
	v_pk_add_f32 v[24:25], v[24:25], v[40:41]
	s_waitcnt vmcnt(0)
	v_pk_add_f32 v[28:29], v[28:29], v[44:45]
	v_cvt_pk_fp8_f32 v48, v20, v21
	v_cvt_pk_fp8_f32 v49, v34, v35
	v_pk_add_f32 v[26:27], v[26:27], v[42:43]
	v_pk_mul_f32 v[38:39], v[100:101], v[24:25]
	v_pk_mul_f32 v[42:43], v[96:97], v[28:29]
	v_cvt_pk_fp8_f32 v50, v38, v39
	v_cvt_pk_fp8_f32 v51, v42, v43
	v_cvt_pk_bf16_f32 v19, v32, v33
	v_pk_mul_f32 v[22:23], v[110:111], v[22:23]
	v_pk_mul_f32 v[32:33], v[106:107], v[32:33]
	v_pk_add_f32 v[30:31], v[30:31], v[46:47]
	v_cvt_pk_fp8_f32 v48, v22, v23 op_sel:[0,0,1]
	v_cvt_pk_fp8_f32 v49, v32, v33 op_sel:[0,0,1]
	v_pk_mul_f32 v[36:37], v[102:103], v[26:27]
	v_pk_mul_f32 v[40:41], v[98:99], v[30:31]
	v_cvt_pk_fp8_f32 v50, v36, v37 op_sel:[0,0,1]
	v_cvt_pk_fp8_f32 v51, v40, v41 op_sel:[0,0,1]
	global_store_dwordx4 v[54:55], v[16:19], off
	global_store_dwordx2 v[56:57], v[48:49], off
	v_mov_b32_e32 v32, 0
	v_cvt_pk_bf16_f32 v16, v24, v25
	v_cvt_pk_bf16_f32 v17, v26, v27
	v_cvt_pk_bf16_f32 v18, v28, v29
	v_cvt_pk_bf16_f32 v19, v30, v31
	global_store_dwordx4 v[54:55], v[16:19], off offset:256
	global_store_dwordx2 v[56:57], v[50:51], off offset:128
	global_load_dwordx4 v[16:19], v[58:59], off nt
	s_nop 0
	global_load_dwordx4 v[20:23], v[58:59], off offset:16 nt
	global_load_dwordx4 v[24:27], v[58:59], off offset:512 nt
	global_load_dwordx4 v[28:31], v[58:59], off offset:528 nt
	v_mov_b32_e32 v33, 0
	v_mov_b32_e32 v34, 0
	v_mov_b32_e32 v35, 0
	v_lshl_add_u64 v[36:37], v[52:53], 1, s[38:39]
	v_lshl_add_u64 v[38:39], s[60:61], 0, v[52:53]
	s_waitcnt vmcnt(3)
	v_pk_add_f32 v[6:7], v[6:7], v[18:19]
	v_pk_add_f32 v[4:5], v[4:5], v[16:17]
	s_waitcnt vmcnt(2)
	v_pk_add_f32 v[18:19], v[0:1], v[20:21]
	v_pk_add_f32 v[16:17], v[2:3], v[22:23]
	v_cvt_pk_bf16_f32 v0, v4, v5
	v_cvt_pk_bf16_f32 v1, v6, v7
	v_cvt_pk_bf16_f32 v2, v18, v19
	v_pk_mul_f32 v[4:5], v[108:109], v[4:5]
	v_pk_mul_f32 v[18:19], v[104:105], v[18:19]
	s_waitcnt vmcnt(1)
	v_pk_add_f32 v[8:9], v[8:9], v[24:25]
	s_waitcnt vmcnt(0)
	v_pk_add_f32 v[12:13], v[12:13], v[28:29]
	v_cvt_pk_fp8_f32 v32, v4, v5
	v_cvt_pk_fp8_f32 v33, v18, v19
	v_pk_add_f32 v[10:11], v[10:11], v[26:27]
	v_pk_mul_f32 v[22:23], v[100:101], v[8:9]
	v_pk_mul_f32 v[26:27], v[96:97], v[12:13]
	v_cvt_pk_fp8_f32 v34, v22, v23
	v_cvt_pk_fp8_f32 v35, v26, v27
	v_cvt_pk_bf16_f32 v3, v16, v17
	v_pk_mul_f32 v[6:7], v[110:111], v[6:7]
	v_pk_mul_f32 v[16:17], v[106:107], v[16:17]
	v_pk_add_f32 v[14:15], v[14:15], v[30:31]
	v_cvt_pk_fp8_f32 v32, v6, v7 op_sel:[0,0,1]
	v_cvt_pk_fp8_f32 v33, v16, v17 op_sel:[0,0,1]
	v_pk_mul_f32 v[20:21], v[102:103], v[10:11]
	v_pk_mul_f32 v[24:25], v[98:99], v[14:15]
	v_cvt_pk_fp8_f32 v34, v20, v21 op_sel:[0,0,1]
	v_cvt_pk_fp8_f32 v35, v24, v25 op_sel:[0,0,1]
	global_store_dwordx4 v[36:37], v[0:3], off
	global_store_dwordx2 v[38:39], v[32:33], off
	s_nop 0
	v_cvt_pk_bf16_f32 v0, v8, v9
	v_cvt_pk_bf16_f32 v1, v10, v11
	v_cvt_pk_bf16_f32 v2, v12, v13
	v_cvt_pk_bf16_f32 v3, v14, v15
	global_store_dwordx4 v[36:37], v[0:3], off offset:256
	global_store_dwordx2 v[38:39], v[34:35], off offset:128
	s_cbranch_vccnz .LBB0_478
	s_andn2_b64 vcc, exec, s[4:5]
	s_cbranch_vccnz .LBB0_477
	s_barrier
	s_branch .LBB0_477

; __global__ void __launch_bounds__(512, 2) hymba_fwd(Args args) {
;     ...
;             int ok = (G == 256) ? 1 : 0, F = 0, rank = 0, mine = 0; const int x = bx & 7, j = bx >> 3;
;             for (int xx = 0; xx < 8; ++xx) { int tx = 0; for (int k = 0; k < 4; ++k) tx += tb[xx + 8 * k + 1] - tb[xx + 8 * k]; if (tx > 12) ok = 0;
;                 int f = 8 * tx - 64; f = f < 0 ? 0 : (f > 32 ? 32 : f);
;                 F += 32 - f; int below = j + (xx < x ? 1 : 0) - f; below = below < 0 ? 0 : (below > 32 - f ? 32 - f : below); rank += below; if (xx == x) mine = (j >= f) ? 1 : 0; }
;             tb[66] = ok; tb[67] = F; tb[68] = mine ? rank : -1;
;             for (int i = 0; i < MAXU; ++i) { int T = -1, e = 0, n = 0;
;                 if (ok) { const int U = i * 32 + j, LT = U >> 3; n = U & 7; int cum = 0;
;                     for (int k = 0; k < 4; ++k) { const int ee = x + 8 * k, t0 = tb[ee], nt = tb[ee + 1] - t0; if (T < 0 && LT < cum + nt) { e = ee; T = t0 + (LT - cum); } cum += nt; } }
;                 else { const int L = i * G + bx; if (L < acc * 8) { T = L >> 3; n = L & 7; for (int k = 1; k < 32; ++k) e += (tb[k] <= T) ? 1 : 0; } }
;                 tb[80 + 4 * i] = T; tb[81 + 4 * i] = e; tb[82 + 4 * i] = n; tb[83 + 4 * i] = T < 0 ? 0 : T - tb[e]; } }
;         __syncthreads();
.LBB0_701:
	s_or_b64 exec, exec, s[6:7]
	s_add_i32 s0, 0, 0x22540
	v_mov_b32_e32 v0, s0
	s_waitcnt lgkmcnt(0)
	s_barrier
	s_add_i32 s6, 0, 0x22508
	v_mov_b32_e32 v1, s6
	ds_read_b32 v1, v1
	s_and_b32 s6, s2, 7
	s_lshr_b32 s7, s2, 3
	s_lshl_b32 s8, s6, 2
	s_add_i32 s8, s8, 0x22400
	v_mov_b32_e32 v2, s8
	ds_read2_b32 v[4:5], v2 offset1:1
	ds_read2_b32 v[6:7], v2 offset0:8 offset1:9
	ds_read2_b32 v[8:9], v2 offset0:16 offset1:17
	ds_read2_b32 v[10:11], v2 offset0:24 offset1:25
	ds_read_b32 v12, v2 offset:132
	ds_read_b32 v13, v2 offset:164
	ds_read_b32 v14, v2 offset:196
	ds_read_b32 v15, v2 offset:228
	s_waitcnt lgkmcnt(0)
	v_readfirstlane_b32 s9, v1
	v_readfirstlane_b32 s10, v4
	v_readfirstlane_b32 s14, v5
	v_readfirstlane_b32 s11, v6
	v_readfirstlane_b32 s15, v7
	v_readfirstlane_b32 s12, v8
	v_readfirstlane_b32 s16, v9
	v_readfirstlane_b32 s13, v10
	v_readfirstlane_b32 s17, v11
	v_readfirstlane_b32 s18, v12
	v_readfirstlane_b32 s19, v13
	v_readfirstlane_b32 s20, v14
	v_readfirstlane_b32 s21, v15
	s_cmp_eq_u32 s9, 0
	s_cbranch_scc1 .Lmo_done
	s_sub_i32 s14, s14, s10
	s_add_i32 s40, s14, -1
	s_lshl_b32 s44, s40, 8
	s_sub_i32 s18, s18, s44
	s_cmp_gt_i32 s14, 0
	s_cselect_b32 s18, s18, -1
	s_max_i32 s40, s40, 0
	s_sub_i32 s15, s15, s11
	s_add_i32 s41, s15, -1
	s_lshl_b32 s44, s41, 8
	s_sub_i32 s19, s19, s44
	s_cmp_gt_i32 s15, 0
	s_cselect_b32 s19, s19, -1
	s_max_i32 s41, s41, 0
	s_sub_i32 s16, s16, s12
	s_add_i32 s42, s16, -1
	s_lshl_b32 s44, s42, 8
	s_sub_i32 s20, s20, s44
	s_cmp_gt_i32 s16, 0
	s_cselect_b32 s20, s20, -1
	s_max_i32 s42, s42, 0
	s_sub_i32 s17, s17, s13
	s_add_i32 s43, s17, -1
	s_lshl_b32 s44, s43, 8
	s_sub_i32 s21, s21, s44
	s_cmp_gt_i32 s17, 0
	s_cselect_b32 s21, s21, -1
	s_max_i32 s43, s43, 0
	s_add_i32 s44, s40, s41
	s_add_i32 s44, s44, s42
	s_add_i32 s44, s44, s43
	s_mov_b32 s45, 0
	s_cmp_gt_i32 s14, 0
	s_addc_u32 s45, s45, 0
	s_cmp_gt_i32 s15, 0
	s_addc_u32 s45, s45, 0
	s_cmp_gt_i32 s16, 0
	s_addc_u32 s45, s45, 0
	s_cmp_gt_i32 s17, 0
	s_addc_u32 s45, s45, 0
	s_mov_b32 s46, 0
	s_cmp_gt_i32 s19, s18
	s_addc_u32 s46, s46, 0
	s_cmp_gt_i32 s20, s18
	s_addc_u32 s46, s46, 0
	s_cmp_gt_i32 s21, s18
	s_addc_u32 s46, s46, 0
	s_mov_b32 s47, 0
	s_cmp_ge_i32 s18, s19
	s_addc_u32 s47, s47, 0
	s_cmp_gt_i32 s20, s19
	s_addc_u32 s47, s47, 0
	s_cmp_gt_i32 s21, s19
	s_addc_u32 s47, s47, 0
	s_mov_b32 s48, 0
	s_cmp_ge_i32 s18, s20
	s_addc_u32 s48, s48, 0
	s_cmp_ge_i32 s19, s20
	s_addc_u32 s48, s48, 0
	s_cmp_gt_i32 s21, s20
	s_addc_u32 s48, s48, 0
	s_mov_b32 s49, 0
	s_cmp_ge_i32 s18, s21
	s_addc_u32 s49, s49, 0
	s_cmp_ge_i32 s19, s21
	s_addc_u32 s49, s49, 0
	s_cmp_ge_i32 s20, s21
	s_addc_u32 s49, s49, 0
	s_mov_b32 s50, 0
.Lmo_loop:
	s_lshl_b32 s51, s50, 5
	s_add_i32 s51, s51, s7
	s_and_b32 s52, s51, 7
	s_lshr_b32 s51, s51, 3
	s_mov_b32 s56, -1
	s_mov_b32 s57, 0
	s_mov_b32 s62, 0
	s_cmp_ge_i32 s51, s44
	s_cbranch_scc1 .Lmo_last
	s_mov_b32 s63, s51
	s_cmp_lt_i32 s63, s40
	s_cbranch_scc1 .Lmo_full0
	s_sub_i32 s63, s63, s40
	s_cmp_lt_i32 s63, s41
	s_cbranch_scc1 .Lmo_full1
	s_sub_i32 s63, s63, s41
	s_cmp_lt_i32 s63, s42
	s_cbranch_scc1 .Lmo_full2
	s_sub_i32 s63, s63, s42
	s_cmp_lt_i32 s63, s43
	s_cbranch_scc1 .Lmo_full3
	s_sub_i32 s63, s63, s43
	s_branch .Lmo_store
.Lmo_full0:
	s_add_i32 s56, s10, s63
	s_mov_b32 s62, s63
	s_add_i32 s57, s6, 0
	s_branch .Lmo_store
.Lmo_full1:
	s_add_i32 s56, s11, s63
	s_mov_b32 s62, s63
	s_add_i32 s57, s6, 8
	s_branch .Lmo_store
.Lmo_full2:
	s_add_i32 s56, s12, s63
	s_mov_b32 s62, s63
	s_add_i32 s57, s6, 16
	s_branch .Lmo_store
.Lmo_full3:
	s_add_i32 s56, s13, s63
	s_mov_b32 s62, s63
	s_add_i32 s57, s6, 24
	s_branch .Lmo_store
.Lmo_last:
	s_sub_i32 s63, s51, s44
	s_cmp_ge_i32 s63, s45
	s_cbranch_scc1 .Lmo_store
	s_cmp_gt_i32 s14, 0
	s_cselect_b32 s66, 1, 0
	s_cmp_eq_u32 s63, s46
	s_cselect_b32 s67, s66, 0
	s_cmp_lg_u32 s67, 0
	s_cbranch_scc1 .Lmo_pick0
	s_cmp_gt_i32 s15, 0
	s_cselect_b32 s66, 1, 0
	s_cmp_eq_u32 s63, s47
	s_cselect_b32 s67, s66, 0
	s_cmp_lg_u32 s67, 0
	s_cbranch_scc1 .Lmo_pick1
	s_cmp_gt_i32 s16, 0
	s_cselect_b32 s66, 1, 0
	s_cmp_eq_u32 s63, s48
	s_cselect_b32 s67, s66, 0
	s_cmp_lg_u32 s67, 0
	s_cbranch_scc1 .Lmo_pick2
	s_cmp_gt_i32 s17, 0
	s_cselect_b32 s66, 1, 0
	s_cmp_eq_u32 s63, s49
	s_cselect_b32 s67, s66, 0
	s_cmp_lg_u32 s67, 0
	s_cbranch_scc1 .Lmo_pick3
	s_branch .Lmo_store
.Lmo_pick0:
	s_add_i32 s62, s14, -1
	s_add_i32 s56, s10, s62
	s_add_i32 s57, s6, 0
	s_branch .Lmo_store
.Lmo_pick1:
	s_add_i32 s62, s15, -1
	s_add_i32 s56, s11, s62
	s_add_i32 s57, s6, 8
	s_branch .Lmo_store
.Lmo_pick2:
	s_add_i32 s62, s16, -1
	s_add_i32 s56, s12, s62
	s_add_i32 s57, s6, 16
	s_branch .Lmo_store
.Lmo_pick3:
	s_add_i32 s62, s17, -1
	s_add_i32 s56, s13, s62
	s_add_i32 s57, s6, 24
	s_branch .Lmo_store
.Lmo_store:
	v_mov_b32_e32 v4, s56
	v_mov_b32_e32 v5, s57
	v_mov_b32_e32 v6, s52
	v_mov_b32_e32 v7, s62
	s_lshl_b32 s63, s50, 4
	s_add_i32 s63, s63, 0x22540
	v_mov_b32_e32 v3, s63
	ds_write_b128 v3, v[4:7]
	s_add_i32 s50, s50, 1
	s_cmp_lt_u32 s50, 3
	s_cbranch_scc1 .Lmo_loop
.Lmo_done:
	s_waitcnt lgkmcnt(0)
	s_barrier
	s_add_i32 s0, 0, 0x22540
	v_mov_b32_e32 v0, s0
	ds_read_b32 v0, v0
	s_waitcnt lgkmcnt(0)
	v_readfirstlane_b32 s6, v0
	s_cmp_gt_i32 s6, -1
	s_cselect_b64 s[0:1], -1, 0
	s_cmp_lt_i32 s6, 0
	s_cbranch_scc1 .LBB0_703
	s_add_i32 s6, 0, 0x22544
	v_mov_b32_e32 v0, s6
	s_add_i32 s6, 0, 0x2254c
	v_mov_b32_e32 v1, s6
	ds_read_b32 v0, v0
	ds_read_b32 v1, v1
	s_waitcnt lgkmcnt(1)
	v_readfirstlane_b32 s18, v0
	s_waitcnt lgkmcnt(0)
	v_readfirstlane_b32 s19, v1
	s_branch .LBB0_704

; #define PG8_STAGE(bufoff, gbase, voff) do { const char* _gb = (const char*)(gbase); asm volatile("" : "+s"(_gb)); _Pragma("unroll") for (int _i = 0; _i < 2; ++_i) { unsigned _vo = (voff)[_i]; asm volatile("" : "+v"(_vo)); \
;         __builtin_amdgcn_global_load_lds((const unsigned*)(_gb + _vo), (LAS unsigned*)(lds + (bufoff) + ldsw + _i * 8192), 16, 0, 0); } } while (0)
; #define PG8_GLOAD(v, slot_) do { const int _t = wid * 64 + lane_id_v(); _Pragma("unroll") for (int _i = 0; _i < 2; ++_i) { int _R, _C; stage_rc(_t * 16 + _i * 8192, _R, _C); \
;         _Pragma("unroll") for (int _h = 0; _h < 2; ++_h) { int _tk = gtok[(slot_) * 256 + 128 * _h + _R]; _tk = _tk < 0 ? 0 : _tk; v[_h][_i] = (unsigned)(_tk * K + _C) * 2u; } } } while (0)
; #define PG8_WAIT_V(n) asm volatile("s_waitcnt vmcnt(" #n ")" ::: "memory")
; #define PG8_WAIT_L(n) asm volatile("s_waitcnt lgkmcnt(" #n ")" ::: "memory")
; #define PG8_BAR __builtin_amdgcn_s_barrier()
; #define PG8_SCHED __builtin_amdgcn_sched_barrier(0)
; template <class Epi, class Sched, bool ALIGN_EPI, bool GATHER, bool F8 = false>
; __device__ __forceinline__ void gemm_phase(LAS unsigned char* lds, const Gemm g, const Sched& S, const Epi& E, const LAS int* gtok, const int tid) {
;     ...
;     for (;;) {
;         const bool has_next = S.next(ui + 1, nxt);
;         const char* nA = GATHER ? cA : (has_next ? (const char*)g.A + (size_t)nxt.pm * tstep : cA); const char* nB = has_next ? (const char*)g.Bt + (size_t)nxt.pn * tstep : cB;
; #pragma unroll 1
;         for (int t = 0; t < nt; t += 2) {
;             const bool last = (t == nt - 2);
;             const char* a1 = cA + (size_t)(t + 1) * kstep;
;             const char* a2 = last ? nA : cA + (size_t)(t + 2) * kstep; const char* b2 = last ? nB : cB + (size_t)(t + 2) * kstep;
;             const char* a3 = a2 + kstep; const char* b3 = b2 + kstep;
;             unsigned vS[2][2];
; #pragma unroll
;             for (int h = 0; h < 2; ++h)
; #pragma unroll
;                 for (int i = 0; i < 2; ++i) vS[h][i] = vA[h][i];
;             if constexpr (GATHER) { if (last && has_next) { PG8_GLOAD(vS, nxt.slot); } }
;             PG8_LDB(B0, 0, 0); PG8_LDB(B1, 0, 1); PG8_SCHED; PG8_LDA(At, 0, 0); PG8_STAGE(PG8_SA(1, 1), a1, vA[1]);
;             PG8_WAIT_V(8); PG8_WAIT_L(0); PG8_BAR; PG8_MMA(0, 0, At, B0); PG8_MMA(0, 1, At, B1); PG8_BAR; PG8_SCHED;
.LBB0_742:
	s_ashr_i32 s9, s8, 31
	s_lshl_b64 s[10:11], s[8:9], 19
	s_add_u32 s10, s35, s10
	s_addc_u32 s11, s53, s11
	s_and_b64 s[18:19], s[12:13], exec
	s_cselect_b32 s67, s11, s17
	s_cselect_b32 s68, s10, s16
	s_lshl_b32 s9, s64, 10
	s_add_i32 s9, s9, 0
	s_add_i32 s9, s9, 0x20000
	s_add_u32 s69, s16, 0x100
	v_mov_b32_e32 v0, 0
	s_addc_u32 s72, s17, 0
	s_mov_b32 s73, -2
	s_mov_b64 s[16:17], s[60:61]
	v_mov_b32_e32 v1, v0
	v_mov_b32_e32 v2, v0
	v_mov_b32_e32 v3, v0
	v_mov_b32_e32 v4, v0
	v_mov_b32_e32 v5, v0
	v_mov_b32_e32 v6, v0
	v_mov_b32_e32 v7, v0
	v_mov_b32_e32 v16, v0
	v_mov_b32_e32 v17, v0
	v_mov_b32_e32 v18, v0
	v_mov_b32_e32 v19, v0
	v_mov_b32_e32 v20, v0
	v_mov_b32_e32 v21, v0
	v_mov_b32_e32 v22, v0
	v_mov_b32_e32 v23, v0
	v_mov_b32_e32 v32, v0
	v_mov_b32_e32 v33, v0
	v_mov_b32_e32 v34, v0
	v_mov_b32_e32 v35, v0
	v_mov_b32_e32 v36, v0
	v_mov_b32_e32 v37, v0
	v_mov_b32_e32 v38, v0
	v_mov_b32_e32 v39, v0
	v_mov_b32_e32 v48, v0
	v_mov_b32_e32 v49, v0
	v_mov_b32_e32 v50, v0
	v_mov_b32_e32 v51, v0
	v_mov_b32_e32 v52, v0
	v_mov_b32_e32 v53, v0
	v_mov_b32_e32 v54, v0
	v_mov_b32_e32 v55, v0
	v_mov_b32_e32 v8, v0
	v_mov_b32_e32 v9, v0
	v_mov_b32_e32 v10, v0
	v_mov_b32_e32 v11, v0
	v_mov_b32_e32 v12, v0
	v_mov_b32_e32 v13, v0
	v_mov_b32_e32 v14, v0
	v_mov_b32_e32 v15, v0
	v_mov_b32_e32 v24, v0
	v_mov_b32_e32 v25, v0
	v_mov_b32_e32 v26, v0
	v_mov_b32_e32 v27, v0
	v_mov_b32_e32 v28, v0
	v_mov_b32_e32 v29, v0
	v_mov_b32_e32 v30, v0
	v_mov_b32_e32 v31, v0
	v_mov_b32_e32 v40, v0
	v_mov_b32_e32 v41, v0
	v_mov_b32_e32 v42, v0
	v_mov_b32_e32 v43, v0
	v_mov_b32_e32 v44, v0
	v_mov_b32_e32 v45, v0
	v_mov_b32_e32 v46, v0
	v_mov_b32_e32 v47, v0
	v_mov_b32_e32 v56, v0
	v_mov_b32_e32 v57, v0
	v_mov_b32_e32 v58, v0
	v_mov_b32_e32 v59, v0
	v_mov_b32_e32 v60, v0
	v_mov_b32_e32 v61, v0
	v_mov_b32_e32 v62, v0
	v_mov_b32_e32 v63, v0
	v_mov_b32_e32 v64, v0
	v_mov_b32_e32 v65, v0
	v_mov_b32_e32 v66, v0
	v_mov_b32_e32 v67, v0
	v_mov_b32_e32 v68, v0
	v_mov_b32_e32 v69, v0
	v_mov_b32_e32 v70, v0
	v_mov_b32_e32 v71, v0
	v_mov_b32_e32 v80, v0
	v_mov_b32_e32 v81, v0
	v_mov_b32_e32 v82, v0
	v_mov_b32_e32 v83, v0
	v_mov_b32_e32 v84, v0
	v_mov_b32_e32 v85, v0
	v_mov_b32_e32 v86, v0
	v_mov_b32_e32 v87, v0
	v_mov_b32_e32 v96, v0
	v_mov_b32_e32 v97, v0
	v_mov_b32_e32 v98, v0
	v_mov_b32_e32 v99, v0
	v_mov_b32_e32 v100, v0
	v_mov_b32_e32 v101, v0
	v_mov_b32_e32 v102, v0
	v_mov_b32_e32 v103, v0
	v_mov_b32_e32 v112, v0
	v_mov_b32_e32 v113, v0
	v_mov_b32_e32 v114, v0
	v_mov_b32_e32 v115, v0
	v_mov_b32_e32 v116, v0
	v_mov_b32_e32 v117, v0
	v_mov_b32_e32 v118, v0
	v_mov_b32_e32 v119, v0
	v_mov_b32_e32 v72, v0
	v_mov_b32_e32 v73, v0
	v_mov_b32_e32 v74, v0
	v_mov_b32_e32 v75, v0
	v_mov_b32_e32 v76, v0
	v_mov_b32_e32 v77, v0
	v_mov_b32_e32 v78, v0
	v_mov_b32_e32 v79, v0
	v_mov_b32_e32 v88, v0
	v_mov_b32_e32 v89, v0
	v_mov_b32_e32 v90, v0
	v_mov_b32_e32 v91, v0
	v_mov_b32_e32 v92, v0
	v_mov_b32_e32 v93, v0
	v_mov_b32_e32 v94, v0
	v_mov_b32_e32 v95, v0
	v_mov_b32_e32 v104, v0
	v_mov_b32_e32 v105, v0
	v_mov_b32_e32 v106, v0
	v_mov_b32_e32 v107, v0
	v_mov_b32_e32 v108, v0
	v_mov_b32_e32 v109, v0
	v_mov_b32_e32 v110, v0
	v_mov_b32_e32 v111, v0
	v_mov_b32_e32 v120, v0
	v_mov_b32_e32 v121, v0
	v_mov_b32_e32 v122, v0
	v_mov_b32_e32 v123, v0
	v_mov_b32_e32 v124, v0
	v_mov_b32_e32 v125, v0
	v_mov_b32_e32 v126, v0
	v_mov_b32_e32 v127, v0
	s_lshr_b32 s100, s14, 3
	s_lshl_b32 s100, s100, 2
	s_add_i32 s100, s100, 0x22400
	v_mov_b32_e32 v206, s100
	ds_read_b32 v207, v206
	ds_read_b32 v206, v206 offset:132
	s_waitcnt lgkmcnt(0)
	v_readfirstlane_b32 s100, v207
	v_readfirstlane_b32 s101, v206
	s_sub_i32 s100, s52, s100
	s_lshl_b32 s100, s100, 8
	s_sub_i32 s101, s101, s100
	s_lshr_b32 s100, s47, 6
	s_lshl_b32 s100, s100, 6
	s_sub_i32 s101, s101, s100
	s_cmp_le_i32 s101, 0
	s_cselect_b32 s99, 1, 0
	s_cmpk_le_i32 s101, 0x80
	s_cselect_b32 s98, 1, 0
	s_branch .LBB0_744
.LBB0_743:
	s_add_u32 s18, s16, 0x100
	s_addc_u32 s19, s17, 0
	s_and_b64 s[20:21], s[22:23], exec
	s_cselect_b32 s36, s60, s18
	v_add_u32_e32 v154, s51, v133
	v_add_u32_e32 v170, s56, v133
	s_cselect_b32 s37, s61, s19
	s_add_u32 s20, s36, 0x80
	ds_read_b128 v[142:145], v154
	ds_read_b128 v[146:149], v154 offset:1024
	ds_read_b128 v[150:153], v154 offset:2048
	ds_read_b128 v[154:157], v154 offset:3072
	ds_read_b128 v[158:161], v170
	ds_read_b128 v[162:165], v170 offset:1024
	ds_read_b128 v[166:169], v170 offset:2048
	ds_read_b128 v[170:173], v170 offset:3072
	s_addc_u32 s21, s37, 0
	s_add_u32 s40, s16, 0x80
	s_addc_u32 s41, s17, 0
	s_and_b64 s[16:17], s[22:23], exec
	s_cselect_b32 s16, s68, s69
	s_cselect_b32 s17, s67, s72
	s_add_u32 s22, s16, 0x80
	s_addc_u32 s23, s17, 0
	v_mov_b32_e32 v206, v129
	ds_read_b128 v[174:177], v134
	ds_read_b128 v[178:181], v134 offset:1024
	ds_read_b128 v[182:185], v134 offset:2048
	ds_read_b128 v[186:189], v134 offset:3072
	ds_read_b128 v[190:193], v134 offset:4096
	ds_read_b128 v[194:197], v134 offset:5120
	ds_read_b128 v[198:201], v134 offset:6144
	ds_read_b128 v[202:205], v134 offset:7168
	s_add_i32 m0, s43, 0xc000
	s_nop 0
	global_load_lds_dwordx4 v206, s[40:41]
	v_mov_b32_e32 v206, v137
	s_add_i32 m0, s43, 0xe000
	s_nop 0
	global_load_lds_dwordx4 v206, s[40:41]
	s_waitcnt vmcnt(8)
	s_waitcnt lgkmcnt(0)
	s_barrier
	s_setprio 1
	s_waitcnt lgkmcnt(0)
	s_cmp_lg_u32 s99, 0
	s_cbranch_scc1 .Lmoe_skip_p5_0
; #define PG8_STAGE(bufoff, gbase, voff) do { const char* _gb = (const char*)(gbase); asm volatile("" : "+s"(_gb)); _Pragma("unroll") for (int _i = 0; _i < 2; ++_i) { unsigned _vo = (voff)[_i]; asm volatile("" : "+v"(_vo)); \
;         __builtin_amdgcn_global_load_lds((const unsigned*)(_gb + _vo), (LAS unsigned*)(lds + (bufoff) + ldsw + _i * 8192), 16, 0, 0); } } while (0)
; #define PG8_WAIT_V(n) asm volatile("s_waitcnt vmcnt(" #n ")" ::: "memory")
; #define PG8_WAIT_L(n) asm volatile("s_waitcnt lgkmcnt(" #n ")" ::: "memory")
; #define PG8_BAR __builtin_amdgcn_s_barrier()
; #define PG8_SCHED __builtin_amdgcn_sched_barrier(0)
; template <class Epi, class Sched, bool ALIGN_EPI, bool GATHER, bool F8 = false>
; __device__ __forceinline__ void gemm_phase(LAS unsigned char* lds, const Gemm g, const Sched& S, const Epi& E, const LAS int* gtok, const int tid) {
;     ...
;             PG8_WAIT_V(8); PG8_WAIT_L(0); PG8_BAR; PG8_MMA(0, 0, At, B0); PG8_MMA(0, 1, At, B1); PG8_BAR; PG8_SCHED;
;             PG8_LDA(At, 0, 1); PG8_STAGE(PG8_SB(0, 0), b2, voffB); PG8_STAGE(PG8_SB(0, 1), b2 + hstep, voffB); PG8_STAGE(PG8_SA(0, 0), a2, vS[0]);
;             PG8_WAIT_V(8); PG8_WAIT_L(0); PG8_BAR; PG8_MMA(1, 0, At, B0); PG8_MMA(1, 1, At, B1); PG8_BAR; PG8_SCHED;
;             PG8_LDB(B0, 1, 0); PG8_LDB(B1, 1, 1); PG8_SCHED; PG8_LDA(At, 1, 0); PG8_STAGE(PG8_SA(0, 1), a2, vS[1]);
	v_mfma_scale_f32_16x16x128_f8f6f4 v[124:127], v[142:149], v[174:181], v[124:127], v135, v135 op_sel_hi:[0,0,0]
	v_mfma_scale_f32_16x16x128_f8f6f4 v[120:123], v[150:157], v[174:181], v[120:123], v135, v135 op_sel_hi:[0,0,0]
	v_mfma_scale_f32_16x16x128_f8f6f4 v[108:111], v[142:149], v[182:189], v[108:111], v135, v135 op_sel_hi:[0,0,0]
	v_mfma_scale_f32_16x16x128_f8f6f4 v[104:107], v[150:157], v[182:189], v[104:107], v135, v135 op_sel_hi:[0,0,0]
	v_mfma_scale_f32_16x16x128_f8f6f4 v[206:209], v[142:149], v[190:197], v[92:95], v135, v135 op_sel_hi:[0,0,0]
	v_mfma_scale_f32_16x16x128_f8f6f4 v[210:213], v[150:157], v[190:197], v[88:91], v135, v135 op_sel_hi:[0,0,0]
	v_mfma_scale_f32_16x16x128_f8f6f4 v[214:217], v[142:149], v[198:205], v[76:79], v135, v135 op_sel_hi:[0,0,0]
	v_mfma_scale_f32_16x16x128_f8f6f4 v[218:221], v[150:157], v[198:205], v[72:75], v135, v135 op_sel_hi:[0,0,0]
	s_setprio 0
	s_setprio 1
	v_mfma_scale_f32_16x16x128_f8f6f4 v[116:119], v[158:165], v[174:181], v[116:119], v135, v135 op_sel_hi:[0,0,0]
	v_mfma_scale_f32_16x16x128_f8f6f4 v[112:115], v[166:173], v[174:181], v[112:115], v135, v135 op_sel_hi:[0,0,0]
	v_mfma_scale_f32_16x16x128_f8f6f4 v[100:103], v[158:165], v[182:189], v[100:103], v135, v135 op_sel_hi:[0,0,0]
	v_mfma_scale_f32_16x16x128_f8f6f4 v[96:99], v[166:173], v[182:189], v[96:99], v135, v135 op_sel_hi:[0,0,0]
	v_mfma_scale_f32_16x16x128_f8f6f4 v[174:177], v[158:165], v[190:197], v[84:87], v135, v135 op_sel_hi:[0,0,0]
	v_mfma_scale_f32_16x16x128_f8f6f4 v[178:181], v[166:173], v[190:197], v[80:83], v135, v135 op_sel_hi:[0,0,0]
	v_mfma_scale_f32_16x16x128_f8f6f4 v[182:185], v[158:165], v[198:205], v[68:71], v135, v135 op_sel_hi:[0,0,0]
	v_mfma_scale_f32_16x16x128_f8f6f4 v[186:189], v[166:173], v[198:205], v[64:67], v135, v135 op_sel_hi:[0,0,0]
.Lmoe_skip_p5_0:
	s_setprio 0
	s_barrier
	s_mov_b64 s[40:41], s[16:17]
	v_mov_b32_e32 v190, v131
	s_add_i32 s33, s51, s42
	s_nop 1
	ds_read_b128 v[64:67], v134 offset:16384
	ds_read_b128 v[68:71], v134 offset:17408
	ds_read_b128 v[72:75], v134 offset:18432
	ds_read_b128 v[76:79], v134 offset:19456
	ds_read_b128 v[80:83], v134 offset:20480
	ds_read_b128 v[84:87], v134 offset:21504
	ds_read_b128 v[88:91], v134 offset:22528
	ds_read_b128 v[92:95], v134 offset:23552
	s_mov_b32 m0, s33
	s_nop 0
	global_load_lds_dwordx4 v190, s[40:41]
	v_mov_b32_e32 v190, v132
	s_add_i32 m0, s33, 0x2000
	s_nop 0
	global_load_lds_dwordx4 v190, s[40:41]
	s_add_u32 s40, s16, 0x40000
	s_addc_u32 s41, s17, 0
	v_mov_b32_e32 v190, v131
	s_add_i32 s33, s56, s42
	s_mov_b32 m0, s33
	s_nop 0
	global_load_lds_dwordx4 v190, s[40:41]
	v_mov_b32_e32 v190, v132
	s_add_i32 m0, s33, 0x2000
	s_nop 0
	global_load_lds_dwordx4 v190, s[40:41]
	s_mov_b64 s[40:41], s[36:37]
	v_mov_b32_e32 v190, v138
	s_mov_b32 m0, s43
	s_nop 0
	global_load_lds_dwordx4 v190, s[40:41]
	v_mov_b32_e32 v190, v139
	s_mov_b32 m0, s44
	s_nop 0
	global_load_lds_dwordx4 v190, s[40:41]
	s_waitcnt vmcnt(8)
	s_waitcnt lgkmcnt(0)
	s_barrier
	s_setprio 1
	s_waitcnt lgkmcnt(0)
	s_cmp_lg_u32 s98, 0
	s_cbranch_scc1 .Lmoe_skip_p5_1
	v_mfma_scale_f32_16x16x128_f8f6f4 v[60:63], v[142:149], v[64:71], v[60:63], v135, v135 op_sel_hi:[0,0,0]
	v_mfma_scale_f32_16x16x128_f8f6f4 v[56:59], v[150:157], v[64:71], v[56:59], v135, v135 op_sel_hi:[0,0,0]
	v_mfma_scale_f32_16x16x128_f8f6f4 v[190:193], v[142:149], v[72:79], v[44:47], v135, v135 op_sel_hi:[0,0,0]
	v_mfma_scale_f32_16x16x128_f8f6f4 v[194:197], v[150:157], v[72:79], v[40:43], v135, v135 op_sel_hi:[0,0,0]
	v_mfma_scale_f32_16x16x128_f8f6f4 v[198:201], v[142:149], v[80:87], v[28:31], v135, v135 op_sel_hi:[0,0,0]
	v_mfma_scale_f32_16x16x128_f8f6f4 v[202:205], v[150:157], v[80:87], v[24:27], v135, v135 op_sel_hi:[0,0,0]
	v_mfma_scale_f32_16x16x128_f8f6f4 v[222:225], v[142:149], v[88:95], v[12:15], v135, v135 op_sel_hi:[0,0,0]
	v_mfma_scale_f32_16x16x128_f8f6f4 v[226:229], v[150:157], v[88:95], v[8:11], v135, v135 op_sel_hi:[0,0,0]
	s_setprio 0
	s_setprio 1
	v_mfma_scale_f32_16x16x128_f8f6f4 v[52:55], v[158:165], v[64:71], v[52:55], v135, v135 op_sel_hi:[0,0,0]
	v_mfma_scale_f32_16x16x128_f8f6f4 v[48:51], v[166:173], v[64:71], v[48:51], v135, v135 op_sel_hi:[0,0,0]
	v_mfma_scale_f32_16x16x128_f8f6f4 v[230:233], v[158:165], v[72:79], v[36:39], v135, v135 op_sel_hi:[0,0,0]
	v_mfma_scale_f32_16x16x128_f8f6f4 v[234:237], v[166:173], v[72:79], v[32:35], v135, v135 op_sel_hi:[0,0,0]
	v_mfma_scale_f32_16x16x128_f8f6f4 v[238:241], v[158:165], v[80:87], v[20:23], v135, v135 op_sel_hi:[0,0,0]
	v_mfma_scale_f32_16x16x128_f8f6f4 v[242:245], v[166:173], v[80:87], v[16:19], v135, v135 op_sel_hi:[0,0,0]
	v_mfma_scale_f32_16x16x128_f8f6f4 v[246:249], v[158:165], v[88:95], v[4:7], v135, v135 op_sel_hi:[0,0,0]
	v_mfma_scale_f32_16x16x128_f8f6f4 v[250:253], v[166:173], v[88:95], v[0:3], v135, v135 op_sel_hi:[0,0,0]
; #define PG8_STAGE(bufoff, gbase, voff) do { const char* _gb = (const char*)(gbase); asm volatile("" : "+s"(_gb)); _Pragma("unroll") for (int _i = 0; _i < 2; ++_i) { unsigned _vo = (voff)[_i]; asm volatile("" : "+v"(_vo)); \
;         __builtin_amdgcn_global_load_lds((const unsigned*)(_gb + _vo), (LAS unsigned*)(lds + (bufoff) + ldsw + _i * 8192), 16, 0, 0); } } while (0)
; #define PG8_WAIT_V(n) asm volatile("s_waitcnt vmcnt(" #n ")" ::: "memory")
; #define PG8_WAIT_L(n) asm volatile("s_waitcnt lgkmcnt(" #n ")" ::: "memory")
; #define PG8_BAR __builtin_amdgcn_s_barrier()
; #define PG8_SCHED __builtin_amdgcn_sched_barrier(0)
; template <class Epi, class Sched, bool ALIGN_EPI, bool GATHER, bool F8 = false>
; __device__ __forceinline__ void gemm_phase(LAS unsigned char* lds, const Gemm g, const Sched& S, const Epi& E, const LAS int* gtok, const int tid) {
;     ...
;             PG8_LDB(B0, 1, 0); PG8_LDB(B1, 1, 1); PG8_SCHED; PG8_LDA(At, 1, 0); PG8_STAGE(PG8_SA(0, 1), a2, vS[1]);
;             PG8_WAIT_V(8); PG8_WAIT_L(0); PG8_BAR; PG8_MMA(0, 0, At, B0); PG8_MMA(0, 1, At, B1); PG8_BAR; PG8_SCHED;
;             PG8_LDA(At, 1, 1); PG8_STAGE(PG8_SB(1, 0), b3, voffB); PG8_STAGE(PG8_SB(1, 1), b3 + hstep, voffB); PG8_STAGE(PG8_SA(1, 0), a3, vS[0]);
;             PG8_WAIT_V(8); PG8_WAIT_L(0); PG8_BAR; PG8_MMA(1, 0, At, B0); PG8_MMA(1, 1, At, B1); PG8_BAR; PG8_SCHED;
;         }
.Lmoe_skip_p5_1:
	s_setprio 0
	s_barrier
	s_add_i32 s33, 0, 0x18000
	v_add_u32_e32 v8, s33, v133
	s_add_i32 s40, 0, 0x1c000
	s_nop 1
	ds_read_b128 v[0:3], v8
	ds_read_b128 v[4:7], v8 offset:1024
	ds_read_b128 v[16:19], v8 offset:2048
	ds_read_b128 v[20:23], v8 offset:3072
	v_add_u32_e32 v8, s40, v133
	ds_read_b128 v[142:145], v8
	ds_read_b128 v[146:149], v8 offset:1024
	ds_read_b128 v[150:153], v8 offset:2048
	ds_read_b128 v[154:157], v8 offset:3072
	s_mov_b32 m0, s45
	ds_read_b128 v[8:11], v134 offset:32768
	ds_read_b128 v[12:15], v134 offset:33792
	ds_read_b128 v[24:27], v134 offset:34816
	ds_read_b128 v[28:31], v134 offset:35840
	ds_read_b128 v[32:35], v134 offset:36864
	ds_read_b128 v[36:39], v134 offset:37888
	ds_read_b128 v[40:43], v134 offset:38912
	ds_read_b128 v[44:47], v134 offset:39936
	s_nop 0
	global_load_lds_dwordx4 v140, s[36:37]
	s_mov_b32 m0, s46
	s_nop 0
	global_load_lds_dwordx4 v141, s[36:37]
	s_waitcnt vmcnt(8)
	s_waitcnt lgkmcnt(0)
	s_barrier
	s_setprio 1
	s_waitcnt lgkmcnt(0)
	s_cmp_lg_u32 s99, 0
	s_cbranch_scc1 .Lmoe_skip_p5_2
	v_mfma_scale_f32_16x16x128_f8f6f4 v[124:127], v[0:7], v[8:15], v[124:127], v135, v135 op_sel_hi:[0,0,0]
	v_mfma_scale_f32_16x16x128_f8f6f4 v[120:123], v[16:23], v[8:15], v[120:123], v135, v135 op_sel_hi:[0,0,0]
	v_mfma_scale_f32_16x16x128_f8f6f4 v[108:111], v[0:7], v[24:31], v[108:111], v135, v135 op_sel_hi:[0,0,0]
	v_mfma_scale_f32_16x16x128_f8f6f4 v[104:107], v[16:23], v[24:31], v[104:107], v135, v135 op_sel_hi:[0,0,0]
	v_mfma_scale_f32_16x16x128_f8f6f4 v[92:95], v[0:7], v[32:39], v[206:209], v135, v135 op_sel_hi:[0,0,0]
	v_mfma_scale_f32_16x16x128_f8f6f4 v[88:91], v[16:23], v[32:39], v[210:213], v135, v135 op_sel_hi:[0,0,0]
	v_mfma_scale_f32_16x16x128_f8f6f4 v[76:79], v[0:7], v[40:47], v[214:217], v135, v135 op_sel_hi:[0,0,0]
	v_mfma_scale_f32_16x16x128_f8f6f4 v[72:75], v[16:23], v[40:47], v[218:221], v135, v135 op_sel_hi:[0,0,0]
	s_setprio 0
	s_setprio 1
	v_mfma_scale_f32_16x16x128_f8f6f4 v[116:119], v[142:149], v[8:15], v[116:119], v135, v135 op_sel_hi:[0,0,0]
	v_mfma_scale_f32_16x16x128_f8f6f4 v[112:115], v[150:157], v[8:15], v[112:115], v135, v135 op_sel_hi:[0,0,0]
	v_mfma_scale_f32_16x16x128_f8f6f4 v[100:103], v[142:149], v[24:31], v[100:103], v135, v135 op_sel_hi:[0,0,0]
	v_mfma_scale_f32_16x16x128_f8f6f4 v[96:99], v[150:157], v[24:31], v[96:99], v135, v135 op_sel_hi:[0,0,0]
	v_mfma_scale_f32_16x16x128_f8f6f4 v[84:87], v[142:149], v[32:39], v[174:177], v135, v135 op_sel_hi:[0,0,0]
	v_mfma_scale_f32_16x16x128_f8f6f4 v[80:83], v[150:157], v[32:39], v[178:181], v135, v135 op_sel_hi:[0,0,0]
	v_mfma_scale_f32_16x16x128_f8f6f4 v[68:71], v[142:149], v[40:47], v[182:185], v135, v135 op_sel_hi:[0,0,0]
	v_mfma_scale_f32_16x16x128_f8f6f4 v[64:67], v[150:157], v[40:47], v[186:189], v135, v135 op_sel_hi:[0,0,0]
.Lmoe_skip_p5_2:
	s_setprio 0
	s_barrier
	v_mov_b32_e32 v8, v131
	s_add_i32 s33, s33, s42
	ds_read_b128 v[32:35], v134 offset:49152
	ds_read_b128 v[36:39], v134 offset:50176
	ds_read_b128 v[158:161], v134 offset:51200
	ds_read_b128 v[162:165], v134 offset:52224
	ds_read_b128 v[166:169], v134 offset:53248
	ds_read_b128 v[170:173], v134 offset:54272
	ds_read_b128 v[174:177], v134 offset:55296
	ds_read_b128 v[178:181], v134 offset:56320
	s_mov_b32 m0, s33
	s_nop 0
	global_load_lds_dwordx4 v8, s[22:23]
	v_mov_b32_e32 v8, v132
	s_add_i32 m0, s33, 0x2000
	s_add_u32 s16, s16, 0x40080
	global_load_lds_dwordx4 v8, s[22:23]
	s_addc_u32 s17, s17, 0
	v_mov_b32_e32 v8, v131
	s_add_i32 s22, s40, s42
	s_mov_b32 m0, s22
	s_nop 0
	global_load_lds_dwordx4 v8, s[16:17]
	v_mov_b32_e32 v8, v132
	s_add_i32 m0, s22, 0x2000
	s_nop 0
	global_load_lds_dwordx4 v8, s[16:17]
	s_mov_b32 m0, s49
	s_nop 0
	global_load_lds_dwordx4 v138, s[20:21]
	s_mov_b32 m0, s50
	s_nop 0
	global_load_lds_dwordx4 v139, s[20:21]
	s_waitcnt vmcnt(8)
	s_waitcnt lgkmcnt(0)
	s_barrier
	s_setprio 1
	s_waitcnt lgkmcnt(0)
	s_cmp_lg_u32 s98, 0
	s_cbranch_scc1 .Lmoe_skip_p5_3
	v_mfma_scale_f32_16x16x128_f8f6f4 v[60:63], v[0:7], v[32:39], v[60:63], v135, v135 op_sel_hi:[0,0,0]
	v_mfma_scale_f32_16x16x128_f8f6f4 v[56:59], v[16:23], v[32:39], v[56:59], v135, v135 op_sel_hi:[0,0,0]
	v_mfma_scale_f32_16x16x128_f8f6f4 v[44:47], v[0:7], v[158:165], v[190:193], v135, v135 op_sel_hi:[0,0,0]
	v_mfma_scale_f32_16x16x128_f8f6f4 v[40:43], v[16:23], v[158:165], v[194:197], v135, v135 op_sel_hi:[0,0,0]
	v_mfma_scale_f32_16x16x128_f8f6f4 v[28:31], v[0:7], v[166:173], v[198:201], v135, v135 op_sel_hi:[0,0,0]
	v_mfma_scale_f32_16x16x128_f8f6f4 v[24:27], v[16:23], v[166:173], v[202:205], v135, v135 op_sel_hi:[0,0,0]
	v_mfma_scale_f32_16x16x128_f8f6f4 v[12:15], v[0:7], v[174:181], v[222:225], v135, v135 op_sel_hi:[0,0,0]
	v_mfma_scale_f32_16x16x128_f8f6f4 v[8:11], v[16:23], v[174:181], v[226:229], v135, v135 op_sel_hi:[0,0,0]
	s_setprio 0
	s_setprio 1
	v_mfma_scale_f32_16x16x128_f8f6f4 v[52:55], v[142:149], v[32:39], v[52:55], v135, v135 op_sel_hi:[0,0,0]
	v_mfma_scale_f32_16x16x128_f8f6f4 v[48:51], v[150:157], v[32:39], v[48:51], v135, v135 op_sel_hi:[0,0,0]
	v_mfma_scale_f32_16x16x128_f8f6f4 v[36:39], v[142:149], v[158:165], v[230:233], v135, v135 op_sel_hi:[0,0,0]
	v_mfma_scale_f32_16x16x128_f8f6f4 v[32:35], v[150:157], v[158:165], v[234:237], v135, v135 op_sel_hi:[0,0,0]
	v_mfma_scale_f32_16x16x128_f8f6f4 v[20:23], v[142:149], v[166:173], v[238:241], v135, v135 op_sel_hi:[0,0,0]
	v_mfma_scale_f32_16x16x128_f8f6f4 v[16:19], v[150:157], v[166:173], v[242:245], v135, v135 op_sel_hi:[0,0,0]
	v_mfma_scale_f32_16x16x128_f8f6f4 v[4:7], v[142:149], v[174:181], v[246:249], v135, v135 op_sel_hi:[0,0,0]
	v_mfma_scale_f32_16x16x128_f8f6f4 v[0:3], v[150:157], v[174:181], v[250:253], v135, v135 op_sel_hi:[0,0,0]
.Lmoe_skip_p5_3:
	s_setprio 0
	s_barrier
	s_add_i32 s73, s73, 2
	s_add_u32 s69, s69, 0x100
	s_addc_u32 s72, s72, 0
	s_cmp_gt_u32 s73, 13
	s_mov_b64 s[16:17], s[18:19]
	s_cbranch_scc1 .LBB0_746

; #define PG8_STAGE(bufoff, gbase, voff) do { const char* _gb = (const char*)(gbase); asm volatile("" : "+s"(_gb)); _Pragma("unroll") for (int _i = 0; _i < 2; ++_i) { unsigned _vo = (voff)[_i]; asm volatile("" : "+v"(_vo)); \
;         __builtin_amdgcn_global_load_lds((const unsigned*)(_gb + _vo), (LAS unsigned*)(lds + (bufoff) + ldsw + _i * 8192), 16, 0, 0); } } while (0)
; #define PG8_GLOAD(v, slot_) do { const int _t = wid * 64 + lane_id_v(); _Pragma("unroll") for (int _i = 0; _i < 2; ++_i) { int _R, _C; stage_rc(_t * 16 + _i * 8192, _R, _C); \
;         _Pragma("unroll") for (int _h = 0; _h < 2; ++_h) { int _tk = gtok[(slot_) * 256 + 128 * _h + _R]; _tk = _tk < 0 ? 0 : _tk; v[_h][_i] = (unsigned)(_tk * K + _C) * 2u; } } } while (0)
; #define PG8_WAIT_V(n) asm volatile("s_waitcnt vmcnt(" #n ")" ::: "memory")
; #define PG8_WAIT_L(n) asm volatile("s_waitcnt lgkmcnt(" #n ")" ::: "memory")
; #define PG8_BAR __builtin_amdgcn_s_barrier()
; #define PG8_SCHED __builtin_amdgcn_sched_barrier(0)
; template <class Epi, class Sched, bool ALIGN_EPI, bool GATHER, bool F8 = false>
; __device__ __forceinline__ void gemm_phase(LAS unsigned char* lds, const Gemm g, const Sched& S, const Epi& E, const LAS int* gtok, const int tid) {
;     ...
;     for (;;) {
;         const bool has_next = S.next(ui + 1, nxt);
;         const char* nA = GATHER ? cA : (has_next ? (const char*)g.A + (size_t)nxt.pm * tstep : cA); const char* nB = has_next ? (const char*)g.Bt + (size_t)nxt.pn * tstep : cB;
; #pragma unroll 1
;         for (int t = 0; t < nt; t += 2) {
;             const bool last = (t == nt - 2);
;             const char* a1 = cA + (size_t)(t + 1) * kstep;
;             const char* a2 = last ? nA : cA + (size_t)(t + 2) * kstep; const char* b2 = last ? nB : cB + (size_t)(t + 2) * kstep;
;             const char* a3 = a2 + kstep; const char* b3 = b2 + kstep;
;             unsigned vS[2][2];
; #pragma unroll
;             for (int h = 0; h < 2; ++h)
; #pragma unroll
;                 for (int i = 0; i < 2; ++i) vS[h][i] = vA[h][i];
;             if constexpr (GATHER) { if (last && has_next) { PG8_GLOAD(vS, nxt.slot); } }
;             PG8_LDB(B0, 0, 0); PG8_LDB(B1, 0, 1); PG8_SCHED; PG8_LDA(At, 0, 0); PG8_STAGE(PG8_SA(1, 1), a1, vA[1]);
;             PG8_WAIT_V(8); PG8_WAIT_L(0); PG8_BAR; PG8_MMA(0, 0, At, B0); PG8_MMA(0, 1, At, B1); PG8_BAR; PG8_SCHED;
.LBB0_847:
	s_ashr_i32 s15, s14, 31
	s_lshl_b64 s[18:19], s[14:15], 18
	s_add_u32 s18, s0, s18
	s_addc_u32 s19, s1, s19
	s_and_b64 s[20:21], s[16:17], exec
	s_cselect_b32 s15, s19, s31
	s_cselect_b32 s56, s18, s30
	s_ashr_i32 s13, s12, 31
	s_lshl_b64 s[20:21], s[12:13], 18
	s_add_u32 s20, s70, s20
	s_addc_u32 s21, s71, s21
	s_and_b64 s[40:41], s[16:17], exec
	s_cselect_b32 s13, s21, s37
	s_cselect_b32 s57, s20, s36
	s_add_u32 s58, s36, 0x100
	v_mov_b32_e32 v12, 0
	s_addc_u32 s59, s37, 0
	s_mov_b32 s60, -2
	v_mov_b32_e32 v13, v12
	v_mov_b32_e32 v14, v12
	v_mov_b32_e32 v15, v12
	v_mov_b32_e32 v20, v12
	v_mov_b32_e32 v21, v12
	v_mov_b32_e32 v22, v12
	v_mov_b32_e32 v23, v12
	v_mov_b32_e32 v44, v12
	v_mov_b32_e32 v45, v12
	v_mov_b32_e32 v46, v12
	v_mov_b32_e32 v47, v12
	v_mov_b32_e32 v52, v12
	v_mov_b32_e32 v53, v12
	v_mov_b32_e32 v54, v12
	v_mov_b32_e32 v55, v12
	v_mov_b32_e32 v0, v12
	v_mov_b32_e32 v1, v12
	v_mov_b32_e32 v2, v12
	v_mov_b32_e32 v3, v12
	v_mov_b32_e32 v4, v12
	v_mov_b32_e32 v5, v12
	v_mov_b32_e32 v6, v12
	v_mov_b32_e32 v7, v12
	v_mov_b32_e32 v8, v12
	v_mov_b32_e32 v9, v12
	v_mov_b32_e32 v10, v12
	v_mov_b32_e32 v11, v12
	v_mov_b32_e32 v16, v12
	v_mov_b32_e32 v17, v12
	v_mov_b32_e32 v18, v12
	v_mov_b32_e32 v19, v12
	v_mov_b32_e32 v32, v12
	v_mov_b32_e32 v33, v12
	v_mov_b32_e32 v34, v12
	v_mov_b32_e32 v35, v12
	v_mov_b32_e32 v40, v12
	v_mov_b32_e32 v41, v12
	v_mov_b32_e32 v42, v12
	v_mov_b32_e32 v43, v12
	v_mov_b32_e32 v56, v12
	v_mov_b32_e32 v57, v12
	v_mov_b32_e32 v58, v12
	v_mov_b32_e32 v59, v12
	v_mov_b32_e32 v60, v12
	v_mov_b32_e32 v61, v12
	v_mov_b32_e32 v62, v12
	v_mov_b32_e32 v63, v12
	v_mov_b32_e32 v64, v12
	v_mov_b32_e32 v65, v12
	v_mov_b32_e32 v66, v12
	v_mov_b32_e32 v67, v12
	v_mov_b32_e32 v68, v12
	v_mov_b32_e32 v69, v12
	v_mov_b32_e32 v70, v12
	v_mov_b32_e32 v71, v12
	v_mov_b32_e32 v80, v12
	v_mov_b32_e32 v81, v12
	v_mov_b32_e32 v82, v12
	v_mov_b32_e32 v83, v12
	v_mov_b32_e32 v84, v12
	v_mov_b32_e32 v85, v12
	v_mov_b32_e32 v86, v12
	v_mov_b32_e32 v87, v12
	v_mov_b32_e32 v96, v12
	v_mov_b32_e32 v97, v12
	v_mov_b32_e32 v98, v12
	v_mov_b32_e32 v99, v12
	v_mov_b32_e32 v100, v12
	v_mov_b32_e32 v101, v12
	v_mov_b32_e32 v102, v12
	v_mov_b32_e32 v103, v12
	v_mov_b32_e32 v112, v12
	v_mov_b32_e32 v113, v12
	v_mov_b32_e32 v114, v12
	v_mov_b32_e32 v115, v12
	v_mov_b32_e32 v116, v12
	v_mov_b32_e32 v117, v12
	v_mov_b32_e32 v118, v12
	v_mov_b32_e32 v119, v12
	v_mov_b32_e32 v72, v12
	v_mov_b32_e32 v73, v12
	v_mov_b32_e32 v74, v12
	v_mov_b32_e32 v75, v12
	v_mov_b32_e32 v76, v12
	v_mov_b32_e32 v77, v12
	v_mov_b32_e32 v78, v12
	v_mov_b32_e32 v79, v12
	v_mov_b32_e32 v88, v12
	v_mov_b32_e32 v89, v12
	v_mov_b32_e32 v90, v12
	v_mov_b32_e32 v91, v12
	v_mov_b32_e32 v92, v12
	v_mov_b32_e32 v93, v12
	v_mov_b32_e32 v94, v12
	v_mov_b32_e32 v95, v12
	v_mov_b32_e32 v104, v12
	v_mov_b32_e32 v105, v12
	v_mov_b32_e32 v106, v12
	v_mov_b32_e32 v107, v12
	v_mov_b32_e32 v108, v12
	v_mov_b32_e32 v109, v12
	v_mov_b32_e32 v110, v12
	v_mov_b32_e32 v111, v12
	v_mov_b32_e32 v120, v12
	v_mov_b32_e32 v121, v12
	v_mov_b32_e32 v122, v12
	v_mov_b32_e32 v123, v12
	v_mov_b32_e32 v124, v12
	v_mov_b32_e32 v125, v12
	v_mov_b32_e32 v126, v12
	v_mov_b32_e32 v127, v12
	v_mov_b32_e32 v36, v12
	v_mov_b32_e32 v37, v12
	v_mov_b32_e32 v38, v12
	v_mov_b32_e32 v39, v12
	v_mov_b32_e32 v48, v12
	v_mov_b32_e32 v49, v12
	v_mov_b32_e32 v50, v12
	v_mov_b32_e32 v51, v12
	v_mov_b32_e32 v24, v12
	v_mov_b32_e32 v25, v12
	v_mov_b32_e32 v26, v12
	v_mov_b32_e32 v27, v12
	v_mov_b32_e32 v28, v12
	v_mov_b32_e32 v29, v12
	v_mov_b32_e32 v30, v12
	v_mov_b32_e32 v31, v12
	s_lshr_b32 s100, s28, 3
	s_lshl_b32 s100, s100, 2
	s_add_i32 s100, s100, 0x22400
	v_mov_b32_e32 v128, s100
	ds_read_b32 v129, v128
	ds_read_b32 v128, v128 offset:132
	s_waitcnt lgkmcnt(0)
	v_readfirstlane_b32 s100, v129
	v_readfirstlane_b32 s101, v128
	s_sub_i32 s100, s22, s100
	s_lshl_b32 s100, s100, 8
	s_sub_i32 s101, s101, s100
	s_lshr_b32 s100, s47, 6
	s_lshl_b32 s100, s100, 6
	s_sub_i32 s101, s101, s100
	s_cmp_le_i32 s101, 0
	s_cselect_b32 s99, 1, 0
	s_cmpk_le_i32 s101, 0x80
	s_cselect_b32 s98, 1, 0
.LBB0_848:
	ds_read_b128 v[144:147], v139
	ds_read_b128 v[148:151], v139 offset:1024
	ds_read_b128 v[152:155], v139 offset:2048
	ds_read_b128 v[156:159], v139 offset:3072
	ds_read_b128 v[160:163], v140
	ds_read_b128 v[164:167], v140 offset:1024
	ds_read_b128 v[168:171], v140 offset:2048
	ds_read_b128 v[172:175], v140 offset:3072
	s_add_u32 s36, s30, 0x100
	s_addc_u32 s37, s31, 0
	s_cmp_eq_u32 s60, 4
	s_cselect_b32 s44, s56, s36
	s_cselect_b32 s45, s15, s37
	s_cselect_b32 s40, s57, s58
	s_cselect_b32 s41, s13, s59
	s_add_u32 s42, s44, 0x80
	s_addc_u32 s43, s45, 0
	s_add_u32 s30, s30, 0x80
	s_addc_u32 s31, s31, 0
	v_mov_b32_e32 v128, v134
	ds_read_b128 v[176:179], v141
	ds_read_b128 v[180:183], v141 offset:1024
	ds_read_b128 v[184:187], v141 offset:2048
	ds_read_b128 v[188:191], v141 offset:3072
	ds_read_b128 v[192:195], v141 offset:4096
	ds_read_b128 v[196:199], v141 offset:5120
	ds_read_b128 v[200:203], v141 offset:6144
	ds_read_b128 v[204:207], v141 offset:7168
	s_add_i32 m0, s23, 0xc000
	s_nop 0
	global_load_lds_dwordx4 v128, s[30:31]
	v_mov_b32_e32 v128, v137
	s_add_i32 m0, s23, 0xe000
	s_nop 0
	global_load_lds_dwordx4 v128, s[30:31]
	s_waitcnt vmcnt(8)
	s_waitcnt lgkmcnt(0)
	s_barrier
	s_setprio 1
	s_waitcnt lgkmcnt(0)
	s_cmp_lg_u32 s99, 0
	s_cbranch_scc1 .Lmoe_skip_p6_0
; #define PG8_STAGE(bufoff, gbase, voff) do { const char* _gb = (const char*)(gbase); asm volatile("" : "+s"(_gb)); _Pragma("unroll") for (int _i = 0; _i < 2; ++_i) { unsigned _vo = (voff)[_i]; asm volatile("" : "+v"(_vo)); \
;         __builtin_amdgcn_global_load_lds((const unsigned*)(_gb + _vo), (LAS unsigned*)(lds + (bufoff) + ldsw + _i * 8192), 16, 0, 0); } } while (0)
; #define PG8_WAIT_V(n) asm volatile("s_waitcnt vmcnt(" #n ")" ::: "memory")
; #define PG8_WAIT_L(n) asm volatile("s_waitcnt lgkmcnt(" #n ")" ::: "memory")
; #define PG8_BAR __builtin_amdgcn_s_barrier()
; #define PG8_SCHED __builtin_amdgcn_sched_barrier(0)
; template <class Epi, class Sched, bool ALIGN_EPI, bool GATHER, bool F8 = false>
; __device__ __forceinline__ void gemm_phase(LAS unsigned char* lds, const Gemm g, const Sched& S, const Epi& E, const LAS int* gtok, const int tid) {
;     ...
;             PG8_WAIT_V(8); PG8_WAIT_L(0); PG8_BAR; PG8_MMA(0, 0, At, B0); PG8_MMA(0, 1, At, B1); PG8_BAR; PG8_SCHED;
;             PG8_LDA(At, 0, 1); PG8_STAGE(PG8_SB(0, 0), b2, voffB); PG8_STAGE(PG8_SB(0, 1), b2 + hstep, voffB); PG8_STAGE(PG8_SA(0, 0), a2, vS[0]);
;             PG8_WAIT_V(8); PG8_WAIT_L(0); PG8_BAR; PG8_MMA(1, 0, At, B0); PG8_MMA(1, 1, At, B1); PG8_BAR; PG8_SCHED;
;             PG8_LDB(B0, 1, 0); PG8_LDB(B1, 1, 1); PG8_SCHED; PG8_LDA(At, 1, 0); PG8_STAGE(PG8_SA(0, 1), a2, vS[1]);
	v_mfma_scale_f32_16x16x128_f8f6f4 v[124:127], v[144:151], v[176:183], v[124:127], v142, v142 op_sel_hi:[0,0,0]
	v_mfma_scale_f32_16x16x128_f8f6f4 v[120:123], v[152:159], v[176:183], v[120:123], v142, v142 op_sel_hi:[0,0,0]
	v_mfma_scale_f32_16x16x128_f8f6f4 v[108:111], v[144:151], v[184:191], v[108:111], v142, v142 op_sel_hi:[0,0,0]
	v_mfma_scale_f32_16x16x128_f8f6f4 v[104:107], v[152:159], v[184:191], v[104:107], v142, v142 op_sel_hi:[0,0,0]
	v_mfma_scale_f32_16x16x128_f8f6f4 v[128:131], v[144:151], v[192:199], v[92:95], v142, v142 op_sel_hi:[0,0,0]
	v_mfma_scale_f32_16x16x128_f8f6f4 v[208:211], v[152:159], v[192:199], v[88:91], v142, v142 op_sel_hi:[0,0,0]
	v_mfma_scale_f32_16x16x128_f8f6f4 v[212:215], v[144:151], v[200:207], v[76:79], v142, v142 op_sel_hi:[0,0,0]
	v_mfma_scale_f32_16x16x128_f8f6f4 v[216:219], v[152:159], v[200:207], v[72:75], v142, v142 op_sel_hi:[0,0,0]
	s_setprio 0
	s_setprio 1
	v_mfma_scale_f32_16x16x128_f8f6f4 v[116:119], v[160:167], v[176:183], v[116:119], v142, v142 op_sel_hi:[0,0,0]
	v_mfma_scale_f32_16x16x128_f8f6f4 v[112:115], v[168:175], v[176:183], v[112:115], v142, v142 op_sel_hi:[0,0,0]
	v_mfma_scale_f32_16x16x128_f8f6f4 v[100:103], v[160:167], v[184:191], v[100:103], v142, v142 op_sel_hi:[0,0,0]
	v_mfma_scale_f32_16x16x128_f8f6f4 v[96:99], v[168:175], v[184:191], v[96:99], v142, v142 op_sel_hi:[0,0,0]
	v_mfma_scale_f32_16x16x128_f8f6f4 v[176:179], v[160:167], v[192:199], v[84:87], v142, v142 op_sel_hi:[0,0,0]
	v_mfma_scale_f32_16x16x128_f8f6f4 v[180:183], v[168:175], v[192:199], v[80:83], v142, v142 op_sel_hi:[0,0,0]
	v_mfma_scale_f32_16x16x128_f8f6f4 v[184:187], v[160:167], v[200:207], v[68:71], v142, v142 op_sel_hi:[0,0,0]
	v_mfma_scale_f32_16x16x128_f8f6f4 v[188:191], v[168:175], v[200:207], v[64:67], v142, v142 op_sel_hi:[0,0,0]
.Lmoe_skip_p6_0:
	s_setprio 0
	s_barrier
	s_mov_b64 s[30:31], s[40:41]
	v_mov_b32_e32 v143, v132
	s_add_i32 s33, s52, s11
	s_nop 1
	ds_read_b128 v[64:67], v141 offset:16384
	ds_read_b128 v[68:71], v141 offset:17408
	ds_read_b128 v[72:75], v141 offset:18432
	ds_read_b128 v[76:79], v141 offset:19456
	ds_read_b128 v[80:83], v141 offset:20480
	ds_read_b128 v[84:87], v141 offset:21504
	ds_read_b128 v[88:91], v141 offset:22528
	ds_read_b128 v[92:95], v141 offset:23552
	s_mov_b32 m0, s33
	s_nop 0
	global_load_lds_dwordx4 v143, s[30:31]
	v_mov_b32_e32 v143, v135
	s_add_i32 m0, s33, 0x2000
	s_nop 0
	global_load_lds_dwordx4 v143, s[30:31]
	s_add_u32 s30, s40, 0x20000
	s_addc_u32 s31, s41, 0
	v_mov_b32_e32 v143, v132
	s_add_i32 s33, s53, s11
	s_mov_b32 m0, s33
	s_nop 0
	global_load_lds_dwordx4 v143, s[30:31]
	v_mov_b32_e32 v143, v135
	s_add_i32 m0, s33, 0x2000
	s_nop 0
	global_load_lds_dwordx4 v143, s[30:31]
	s_mov_b64 s[30:31], s[44:45]
	v_mov_b32_e32 v143, v133
	s_mov_b32 m0, s23
	s_nop 0
	global_load_lds_dwordx4 v143, s[30:31]
	v_mov_b32_e32 v143, v136
	s_mov_b32 m0, s29
	s_nop 0
	global_load_lds_dwordx4 v143, s[30:31]
	s_waitcnt vmcnt(8)
	s_waitcnt lgkmcnt(0)
	s_barrier
	s_setprio 1
	s_waitcnt lgkmcnt(0)
	s_cmp_lg_u32 s98, 0
	s_cbranch_scc1 .Lmoe_skip_p6_1
	v_mfma_scale_f32_16x16x128_f8f6f4 v[60:63], v[144:151], v[64:71], v[60:63], v142, v142 op_sel_hi:[0,0,0]
	v_mfma_scale_f32_16x16x128_f8f6f4 v[56:59], v[152:159], v[64:71], v[56:59], v142, v142 op_sel_hi:[0,0,0]
	v_mfma_scale_f32_16x16x128_f8f6f4 v[16:19], v[144:151], v[80:87], v[16:19], v142, v142 op_sel_hi:[0,0,0]
	v_mfma_scale_f32_16x16x128_f8f6f4 v[192:195], v[144:151], v[72:79], v[40:43], v142, v142 op_sel_hi:[0,0,0]
	v_mfma_scale_f32_16x16x128_f8f6f4 v[196:199], v[152:159], v[72:79], v[32:35], v142, v142 op_sel_hi:[0,0,0]
	v_mfma_scale_f32_16x16x128_f8f6f4 v[200:203], v[152:159], v[80:87], v[8:11], v142, v142 op_sel_hi:[0,0,0]
	v_mfma_scale_f32_16x16x128_f8f6f4 v[204:207], v[144:151], v[88:95], v[4:7], v142, v142 op_sel_hi:[0,0,0]
	v_mfma_scale_f32_16x16x128_f8f6f4 v[220:223], v[152:159], v[88:95], v[0:3], v142, v142 op_sel_hi:[0,0,0]
	s_setprio 0
	s_setprio 1
	v_mfma_scale_f32_16x16x128_f8f6f4 v[52:55], v[160:167], v[64:71], v[52:55], v142, v142 op_sel_hi:[0,0,0]
	v_mfma_scale_f32_16x16x128_f8f6f4 v[224:227], v[168:175], v[64:71], v[44:47], v142, v142 op_sel_hi:[0,0,0]
	v_mfma_scale_f32_16x16x128_f8f6f4 v[228:231], v[160:167], v[72:79], v[20:23], v142, v142 op_sel_hi:[0,0,0]
	v_mfma_scale_f32_16x16x128_f8f6f4 v[232:235], v[168:175], v[72:79], v[12:15], v142, v142 op_sel_hi:[0,0,0]
	v_mfma_scale_f32_16x16x128_f8f6f4 v[236:239], v[160:167], v[80:87], v[36:39], v142, v142 op_sel_hi:[0,0,0]
	v_mfma_scale_f32_16x16x128_f8f6f4 v[240:243], v[168:175], v[80:87], v[48:51], v142, v142 op_sel_hi:[0,0,0]
	v_mfma_scale_f32_16x16x128_f8f6f4 v[244:247], v[160:167], v[88:95], v[24:27], v142, v142 op_sel_hi:[0,0,0]
	v_mfma_scale_f32_16x16x128_f8f6f4 v[248:251], v[168:175], v[88:95], v[28:31], v142, v142 op_sel_hi:[0,0,0]
; #define PG8_STAGE(bufoff, gbase, voff) do { const char* _gb = (const char*)(gbase); asm volatile("" : "+s"(_gb)); _Pragma("unroll") for (int _i = 0; _i < 2; ++_i) { unsigned _vo = (voff)[_i]; asm volatile("" : "+v"(_vo)); \
;         __builtin_amdgcn_global_load_lds((const unsigned*)(_gb + _vo), (LAS unsigned*)(lds + (bufoff) + ldsw + _i * 8192), 16, 0, 0); } } while (0)
; #define PG8_WAIT_V(n) asm volatile("s_waitcnt vmcnt(" #n ")" ::: "memory")
; #define PG8_WAIT_L(n) asm volatile("s_waitcnt lgkmcnt(" #n ")" ::: "memory")
; #define PG8_BAR __builtin_amdgcn_s_barrier()
; #define PG8_SCHED __builtin_amdgcn_sched_barrier(0)
; template <class Epi, class Sched, bool ALIGN_EPI, bool GATHER, bool F8 = false>
; __device__ __forceinline__ void gemm_phase(LAS unsigned char* lds, const Gemm g, const Sched& S, const Epi& E, const LAS int* gtok, const int tid) {
;     ...
;             PG8_LDB(B0, 1, 0); PG8_LDB(B1, 1, 1); PG8_SCHED; PG8_LDA(At, 1, 0); PG8_STAGE(PG8_SA(0, 1), a2, vS[1]);
;             PG8_WAIT_V(8); PG8_WAIT_L(0); PG8_BAR; PG8_MMA(0, 0, At, B0); PG8_MMA(0, 1, At, B1); PG8_BAR; PG8_SCHED;
;             PG8_LDA(At, 1, 1); PG8_STAGE(PG8_SB(1, 0), b3, voffB); PG8_STAGE(PG8_SB(1, 1), b3 + hstep, voffB); PG8_STAGE(PG8_SA(1, 0), a3, vS[0]);
;             PG8_WAIT_V(8); PG8_WAIT_L(0); PG8_BAR; PG8_MMA(1, 0, At, B0); PG8_MMA(1, 1, At, B1); PG8_BAR; PG8_SCHED;
;         }
;         if constexpr (ALIGN_EPI) { if (wr == 0) PG8_BAR; }
.Lmoe_skip_p6_1:
	s_setprio 0
	s_barrier
	s_add_i32 s33, 0, 0x18000
	v_add_u32_e32 v8, s33, v138
	s_add_i32 s54, 0, 0x1c000
	ds_read_b128 v[0:3], v8
	ds_read_b128 v[4:7], v8 offset:1024
	ds_read_b128 v[20:23], v8 offset:2048
	ds_read_b128 v[24:27], v8 offset:3072
	v_add_u32_e32 v8, s54, v138
	ds_read_b128 v[144:147], v8
	ds_read_b128 v[148:151], v8 offset:1024
	ds_read_b128 v[152:155], v8 offset:2048
	ds_read_b128 v[156:159], v8 offset:3072
	v_mov_b32_e32 v64, v134
	s_mov_b32 m0, s35
	ds_read_b128 v[8:11], v141 offset:32768
	ds_read_b128 v[12:15], v141 offset:33792
	ds_read_b128 v[28:31], v141 offset:34816
	ds_read_b128 v[32:35], v141 offset:35840
	ds_read_b128 v[36:39], v141 offset:36864
	ds_read_b128 v[40:43], v141 offset:37888
	ds_read_b128 v[44:47], v141 offset:38912
	ds_read_b128 v[48:51], v141 offset:39936
	s_nop 0
	global_load_lds_dwordx4 v64, s[44:45]
	v_mov_b32_e32 v64, v137
	s_mov_b32 m0, s46
	s_nop 0
	global_load_lds_dwordx4 v64, s[44:45]
	s_waitcnt vmcnt(8)
	s_waitcnt lgkmcnt(0)
	s_barrier
	s_setprio 1
	s_waitcnt lgkmcnt(0)
	s_cmp_lg_u32 s99, 0
	s_cbranch_scc1 .Lmoe_skip_p6_2
	v_mfma_scale_f32_16x16x128_f8f6f4 v[124:127], v[0:7], v[8:15], v[124:127], v142, v142 op_sel_hi:[0,0,0]
	v_mfma_scale_f32_16x16x128_f8f6f4 v[120:123], v[20:27], v[8:15], v[120:123], v142, v142 op_sel_hi:[0,0,0]
	v_mfma_scale_f32_16x16x128_f8f6f4 v[108:111], v[0:7], v[28:35], v[108:111], v142, v142 op_sel_hi:[0,0,0]
	v_mfma_scale_f32_16x16x128_f8f6f4 v[104:107], v[20:27], v[28:35], v[104:107], v142, v142 op_sel_hi:[0,0,0]
	v_mfma_scale_f32_16x16x128_f8f6f4 v[92:95], v[0:7], v[36:43], v[128:131], v142, v142 op_sel_hi:[0,0,0]
	v_mfma_scale_f32_16x16x128_f8f6f4 v[88:91], v[20:27], v[36:43], v[208:211], v142, v142 op_sel_hi:[0,0,0]
	v_mfma_scale_f32_16x16x128_f8f6f4 v[76:79], v[0:7], v[44:51], v[212:215], v142, v142 op_sel_hi:[0,0,0]
	v_mfma_scale_f32_16x16x128_f8f6f4 v[72:75], v[20:27], v[44:51], v[216:219], v142, v142 op_sel_hi:[0,0,0]
	s_setprio 0
	s_setprio 1
	v_mfma_scale_f32_16x16x128_f8f6f4 v[116:119], v[144:151], v[8:15], v[116:119], v142, v142 op_sel_hi:[0,0,0]
	v_mfma_scale_f32_16x16x128_f8f6f4 v[112:115], v[152:159], v[8:15], v[112:115], v142, v142 op_sel_hi:[0,0,0]
	v_mfma_scale_f32_16x16x128_f8f6f4 v[100:103], v[144:151], v[28:35], v[100:103], v142, v142 op_sel_hi:[0,0,0]
	v_mfma_scale_f32_16x16x128_f8f6f4 v[96:99], v[152:159], v[28:35], v[96:99], v142, v142 op_sel_hi:[0,0,0]
	v_mfma_scale_f32_16x16x128_f8f6f4 v[84:87], v[144:151], v[36:43], v[176:179], v142, v142 op_sel_hi:[0,0,0]
	v_mfma_scale_f32_16x16x128_f8f6f4 v[80:83], v[152:159], v[36:43], v[180:183], v142, v142 op_sel_hi:[0,0,0]
	v_mfma_scale_f32_16x16x128_f8f6f4 v[68:71], v[144:151], v[44:51], v[184:187], v142, v142 op_sel_hi:[0,0,0]
	v_mfma_scale_f32_16x16x128_f8f6f4 v[64:67], v[152:159], v[44:51], v[188:191], v142, v142 op_sel_hi:[0,0,0]
.Lmoe_skip_p6_2:
	s_setprio 0
	s_barrier
	s_add_u32 s30, s40, 0x80
	s_addc_u32 s31, s41, 0
	v_mov_b32_e32 v8, v132
	s_add_i32 s33, s33, s11
	ds_read_b128 v[44:47], v141 offset:49152
	ds_read_b128 v[48:51], v141 offset:50176
	ds_read_b128 v[160:163], v141 offset:51200
	ds_read_b128 v[164:167], v141 offset:52224
	ds_read_b128 v[168:171], v141 offset:53248
	ds_read_b128 v[172:175], v141 offset:54272
	ds_read_b128 v[176:179], v141 offset:55296
	ds_read_b128 v[180:183], v141 offset:56320
	s_mov_b32 m0, s33
	s_nop 0
	global_load_lds_dwordx4 v8, s[30:31]
	v_mov_b32_e32 v8, v135
	s_add_i32 m0, s33, 0x2000
	s_nop 0
	global_load_lds_dwordx4 v8, s[30:31]
	s_add_u32 s30, s40, 0x20080
	s_addc_u32 s31, s41, 0
	v_mov_b32_e32 v8, v132
	s_add_i32 s33, s54, s11
	s_mov_b32 m0, s33
	s_nop 0
	global_load_lds_dwordx4 v8, s[30:31]
	v_mov_b32_e32 v8, v135
	s_add_i32 m0, s33, 0x2000
	s_nop 0
	global_load_lds_dwordx4 v8, s[30:31]
	v_mov_b32_e32 v8, v133
	s_mov_b32 m0, s49
	s_nop 0
	global_load_lds_dwordx4 v8, s[42:43]
	v_mov_b32_e32 v8, v136
	s_mov_b32 m0, s50
	s_nop 0
	global_load_lds_dwordx4 v8, s[42:43]
	s_waitcnt vmcnt(8)
	s_waitcnt lgkmcnt(0)
	s_barrier
	s_setprio 1
	s_waitcnt lgkmcnt(0)
	s_cmp_lg_u32 s98, 0
	s_cbranch_scc1 .Lmoe_skip_p6_3
	v_mfma_scale_f32_16x16x128_f8f6f4 v[60:63], v[0:7], v[44:51], v[60:63], v142, v142 op_sel_hi:[0,0,0]
	v_mfma_scale_f32_16x16x128_f8f6f4 v[56:59], v[20:27], v[44:51], v[56:59], v142, v142 op_sel_hi:[0,0,0]
	v_mfma_scale_f32_16x16x128_f8f6f4 v[40:43], v[0:7], v[160:167], v[192:195], v142, v142 op_sel_hi:[0,0,0]
	v_mfma_scale_f32_16x16x128_f8f6f4 v[32:35], v[20:27], v[160:167], v[196:199], v142, v142 op_sel_hi:[0,0,0]
	v_mfma_scale_f32_16x16x128_f8f6f4 v[16:19], v[0:7], v[168:175], v[16:19], v142, v142 op_sel_hi:[0,0,0]
	v_mfma_scale_f32_16x16x128_f8f6f4 v[8:11], v[20:27], v[168:175], v[200:203], v142, v142 op_sel_hi:[0,0,0]
	v_mfma_scale_f32_16x16x128_f8f6f4 v[4:7], v[0:7], v[176:183], v[204:207], v142, v142 op_sel_hi:[0,0,0]
	v_mfma_scale_f32_16x16x128_f8f6f4 v[0:3], v[20:27], v[176:183], v[220:223], v142, v142 op_sel_hi:[0,0,0]
	s_setprio 0
	s_setprio 1
	v_mfma_scale_f32_16x16x128_f8f6f4 v[52:55], v[144:151], v[44:51], v[52:55], v142, v142 op_sel_hi:[0,0,0]
	v_mfma_scale_f32_16x16x128_f8f6f4 v[44:47], v[152:159], v[44:51], v[224:227], v142, v142 op_sel_hi:[0,0,0]
	v_mfma_scale_f32_16x16x128_f8f6f4 v[20:23], v[144:151], v[160:167], v[228:231], v142, v142 op_sel_hi:[0,0,0]
	v_mfma_scale_f32_16x16x128_f8f6f4 v[12:15], v[152:159], v[160:167], v[232:235], v142, v142 op_sel_hi:[0,0,0]
	v_mfma_scale_f32_16x16x128_f8f6f4 v[36:39], v[144:151], v[168:175], v[236:239], v142, v142 op_sel_hi:[0,0,0]
	v_mfma_scale_f32_16x16x128_f8f6f4 v[48:51], v[152:159], v[168:175], v[240:243], v142, v142 op_sel_hi:[0,0,0]
	v_mfma_scale_f32_16x16x128_f8f6f4 v[24:27], v[144:151], v[176:183], v[244:247], v142, v142 op_sel_hi:[0,0,0]
	v_mfma_scale_f32_16x16x128_f8f6f4 v[28:31], v[152:159], v[176:183], v[248:251], v142, v142 op_sel_hi:[0,0,0]
.Lmoe_skip_p6_3:
	s_setprio 0
	s_barrier
	s_add_i32 s60, s60, 2
	s_add_u32 s58, s58, 0x100
	s_addc_u32 s59, s59, 0
	s_cmp_gt_u32 s60, 5
	s_mov_b64 s[30:31], s[36:37]
	s_cbranch_scc0 .LBB0_848
	s_and_b64 vcc, exec, s[8:9]
	s_cbranch_vccz .LBB0_851
	s_barrier

; __global__ void __launch_bounds__(512, 2) hymba_fwd(Args args) {
	.amdhsa_kernel _Z9hymba_fwd4Args
		.amdhsa_group_segment_fixed_size 0
		.amdhsa_private_segment_fixed_size 0
		.amdhsa_kernarg_size 440
		.amdhsa_user_sgpr_count 2
		.amdhsa_user_sgpr_dispatch_ptr 0
		.amdhsa_user_sgpr_queue_ptr 0
		.amdhsa_user_sgpr_kernarg_segment_ptr 1
		.amdhsa_user_sgpr_dispatch_id 0
		.amdhsa_user_sgpr_kernarg_preload_length 0
		.amdhsa_user_sgpr_kernarg_preload_offset 0
		.amdhsa_user_sgpr_private_segment_size 0
		.amdhsa_uses_dynamic_stack 0
		.amdhsa_enable_private_segment 0
		.amdhsa_system_sgpr_workgroup_id_x 1
		.amdhsa_system_sgpr_workgroup_id_y 0
		.amdhsa_system_sgpr_workgroup_id_z 0
		.amdhsa_system_sgpr_workgroup_info 0
		.amdhsa_system_vgpr_workitem_id 0
		.amdhsa_next_free_vgpr 256
		.amdhsa_next_free_sgpr 102
		.amdhsa_accum_offset 256
		.amdhsa_reserve_vcc 1
		.amdhsa_float_round_mode_32 0
		.amdhsa_float_round_mode_16_64 0
		.amdhsa_float_denorm_mode_32 3
		.amdhsa_float_denorm_mode_16_64 3
		.amdhsa_dx10_clamp 1
		.amdhsa_ieee_mode 1
		.amdhsa_fp16_overflow 0
		.amdhsa_tg_split 0
		.amdhsa_exception_fp_ieee_invalid_op 0
		.amdhsa_exception_fp_denorm_src 0
		.amdhsa_exception_fp_ieee_div_zero 0
		.amdhsa_exception_fp_ieee_overflow 0
		.amdhsa_exception_fp_ieee_underflow 0
		.amdhsa_exception_fp_ieee_inexact 0
		.amdhsa_exception_int_div_zero 0
	.end_amdhsa_kernel

; __global__ void __launch_bounds__(512, 2) hymba_fwd(Args args) {
amdhsa.kernels:
  - .agpr_count:     0
    .args:
      - .offset:         0
        .size:           184
        .value_kind:     by_value
      - .offset:         184
        .size:           4
        .value_kind:     hidden_block_count_x
      - .offset:         188
        .size:           4
        .value_kind:     hidden_block_count_y
      - .offset:         192
        .size:           4
        .value_kind:     hidden_block_count_z
      - .offset:         196
        .size:           2
        .value_kind:     hidden_group_size_x
      - .offset:         198
        .size:           2
        .value_kind:     hidden_group_size_y
      - .offset:         200
        .size:           2
        .value_kind:     hidden_group_size_z
      - .offset:         202
        .size:           2
        .value_kind:     hidden_remainder_x
      - .offset:         204
        .size:           2
        .value_kind:     hidden_remainder_y
      - .offset:         206
        .size:           2
        .value_kind:     hidden_remainder_z
      - .offset:         224
        .size:           8
        .value_kind:     hidden_global_offset_x
      - .offset:         232
        .size:           8
        .value_kind:     hidden_global_offset_y
      - .offset:         240
        .size:           8
        .value_kind:     hidden_global_offset_z
      - .offset:         248
        .size:           2
        .value_kind:     hidden_grid_dims
      - .offset:         304
        .size:           4
        .value_kind:     hidden_dynamic_lds_size
    .group_segment_fixed_size: 0
    .kernarg_segment_align: 8
    .kernarg_segment_size: 440
    .language:       OpenCL C
    .language_version:
      - 2
      - 0
    .max_flat_workgroup_size: 512
    .name:           _Z9hymba_fwd4Args
    .private_segment_fixed_size: 0
    .sgpr_count:     108
    .sgpr_spill_count: 14
    .symbol:         _Z9hymba_fwd4Args.kd
    .uniform_work_group_size: 1
    .uses_dynamic_stack: false
    .vgpr_count:     256
    .vgpr_spill_count: 0
    .wavefront_size: 64
